# LN1 g/b fragments loaded once per wave; out-GEMM residual fragments prefetched with counted waits; gate-up row indices loaded a K-loop early
# speedup vs baseline: 1.0170x; 1.0030x over previous
; __device__ __forceinline__ unsigned cvt_pk_bf16(float lo, float hi) { typedef __bf16 bf16x2_t __attribute__((ext_vector_type(2))); f32x2 v = {lo, hi}; bf16x2_t b = __builtin_convertvector(v, bf16x2_t); return __builtin_bit_cast(unsigned, b); }
;     __device__ __forceinline__ void operator()(const f32x4 (&acc)[2][2][4][2], const Unit& u, int wr, int wc, int fr, int fq) const {
;         const int row0 = u.pm * BM + wr * 64 + fr, col0 = u.pn * BM + wc * 64 + 16 * fq;
; #pragma unroll
;         for (int ai = 0; ai < 2; ++ai)
; #pragma unroll
;             for (int m = 0; m < 4; ++m) { const size_t off = (size_t)(row0 + ai * HALF + m * 16) * ldc + col0;
;                 const u32x4 ra = *(const u32x4*)(R + off), rb = *(const u32x4*)(R + off + 8);
;                 const f32x4 v0 = acc[ai][0][m][0], v1 = acc[ai][0][m][1], v2 = acc[ai][1][m][0], v3 = acc[ai][1][m][1];
;                 u32x4 wa, wb;
;                 wa.x = cvt_pk_bf16(bflo(ra.x) * alpha + v0[0], bfhi(ra.x) * alpha + v0[1]); wa.y = cvt_pk_bf16(bflo(ra.y) * alpha + v0[2], bfhi(ra.y) * alpha + v0[3]);
;                 wa.z = cvt_pk_bf16(bflo(ra.z) * alpha + v1[0], bfhi(ra.z) * alpha + v1[1]); wa.w = cvt_pk_bf16(bflo(ra.w) * alpha + v1[2], bfhi(ra.w) * alpha + v1[3]);
;                 wb.x = cvt_pk_bf16(bflo(rb.x) * alpha + v2[0], bfhi(rb.x) * alpha + v2[1]); wb.y = cvt_pk_bf16(bflo(rb.y) * alpha + v2[2], bfhi(rb.y) * alpha + v2[3]);
;                 wb.z = cvt_pk_bf16(bflo(rb.z) * alpha + v3[0], bfhi(rb.z) * alpha + v3[1]); wb.w = cvt_pk_bf16(bflo(rb.w) * alpha + v3[2], bfhi(rb.w) * alpha + v3[3]);
;                 *(u32x4*)(O + off) = wa; *(u32x4*)(O + off + 8) = wb; }
.LBB0_732:
	v_lshl_add_u32 v132, s60, 8, v237
	v_lshl_add_u32 v130, s73, 8, v239
	v_ashrrev_i32_e32 v133, 31, v132
	v_ashrrev_i32_e32 v131, 31, v130
	v_lshlrev_b64 v[128:129], 11, v[132:133]
	v_lshl_add_u64 v[128:129], v[128:129], 0, v[130:131]
	v_lshlrev_b64 v[128:129], 1, v[128:129]
	v_lshl_add_u64 v[138:139], s[46:47], 0, v[128:129]
	global_load_dwordx4 v[144:147], v[138:139], off offset:16
	global_load_dwordx4 v[148:151], v[138:139], off
	s_mov_b64 s[8:9], 0x10000
	v_lshl_add_u64 v[244:245], v[138:139], 0, s[8:9]
	global_load_dwordx4 v[152:155], v[244:245], off offset:16
	global_load_dwordx4 v[156:159], v[244:245], off
	s_mov_b64 s[8:9], 0x20000
	v_lshl_add_u64 v[244:245], v[138:139], 0, s[8:9]
	global_load_dwordx4 v[160:163], v[244:245], off offset:16
	global_load_dwordx4 v[164:167], v[244:245], off
	s_mov_b64 s[8:9], 0x30000
	v_lshl_add_u64 v[244:245], v[138:139], 0, s[8:9]
	global_load_dwordx4 v[168:171], v[244:245], off offset:16
	global_load_dwordx4 v[172:175], v[244:245], off
	s_mov_b64 s[8:9], 0x80000
	v_lshl_add_u64 v[244:245], v[138:139], 0, s[8:9]
	global_load_dwordx4 v[176:179], v[244:245], off offset:16
	global_load_dwordx4 v[180:183], v[244:245], off
	s_mov_b64 s[8:9], 0x90000
	v_lshl_add_u64 v[244:245], v[138:139], 0, s[8:9]
	global_load_dwordx4 v[184:187], v[244:245], off offset:16
	global_load_dwordx4 v[188:191], v[244:245], off
	s_mov_b64 s[8:9], 0xa0000
	v_lshl_add_u64 v[246:247], v[138:139], 0, s[8:9]
	s_mov_b64 s[8:9], 0xb0000
	v_lshl_add_u64 v[248:249], v[138:139], 0, s[8:9]
	s_nop 0
	s_mov_b64 s[8:9], 0x80000
	s_andn2_b64 vcc, exec, s[36:37]
	s_waitcnt vmcnt(10)
	v_mov_b64_e32 v[134:135], v[144:145]
	v_mov_b64_e32 v[136:137], v[146:147]
	v_mov_b64_e32 v[138:139], v[148:149]
	v_mov_b64_e32 v[140:141], v[150:151]
	v_lshlrev_b32_e32 v142, 16, v138
	v_and_b32_e32 v143, 0xffff0000, v138
	v_lshlrev_b32_e32 v138, 16, v139
	v_and_b32_e32 v139, 0xffff0000, v139
	v_pk_fma_f32 v[124:125], v[142:143], s[70:71], v[124:125] op_sel_hi:[1,0,1]
	v_pk_fma_f32 v[126:127], v[138:139], s[70:71], v[126:127] op_sel_hi:[1,0,1]
	v_cvt_pk_bf16_f32 v124, v124, v125
	v_cvt_pk_bf16_f32 v125, v126, v127
	v_lshlrev_b32_e32 v126, 16, v140
	v_and_b32_e32 v127, 0xffff0000, v140
	v_pk_fma_f32 v[120:121], v[126:127], s[70:71], v[120:121] op_sel_hi:[1,0,1]
	s_nop 0
	v_cvt_pk_bf16_f32 v126, v120, v121
	v_lshlrev_b32_e32 v120, 16, v141
	v_and_b32_e32 v121, 0xffff0000, v141
	v_pk_fma_f32 v[120:121], v[120:121], s[70:71], v[122:123] op_sel_hi:[1,0,1]
	s_nop 0
	v_cvt_pk_bf16_f32 v127, v120, v121
	v_lshlrev_b32_e32 v120, 16, v134
	v_and_b32_e32 v121, 0xffff0000, v134
	v_pk_fma_f32 v[116:117], v[120:121], s[70:71], v[116:117] op_sel_hi:[1,0,1]
	v_lshlrev_b32_e32 v120, 16, v135
	v_and_b32_e32 v121, 0xffff0000, v135
	v_pk_fma_f32 v[118:119], v[120:121], s[70:71], v[118:119] op_sel_hi:[1,0,1]
	v_cvt_pk_bf16_f32 v116, v116, v117
	v_cvt_pk_bf16_f32 v117, v118, v119
	v_lshlrev_b32_e32 v118, 16, v136
	v_and_b32_e32 v119, 0xffff0000, v136
	v_pk_fma_f32 v[112:113], v[118:119], s[70:71], v[112:113] op_sel_hi:[1,0,1]
	s_nop 0
	v_cvt_pk_bf16_f32 v118, v112, v113
	v_lshlrev_b32_e32 v112, 16, v137
	v_and_b32_e32 v113, 0xffff0000, v137
	v_pk_fma_f32 v[112:113], v[112:113], s[70:71], v[114:115] op_sel_hi:[1,0,1]
	s_nop 0
	v_cvt_pk_bf16_f32 v119, v112, v113
	v_lshl_add_u64 v[112:113], s[44:45], 0, v[128:129]
	global_store_dwordx4 v[112:113], v[124:127], off
	global_store_dwordx4 v[112:113], v[116:119], off offset:16
	v_or_b32_e32 v112, 16, v132
	v_ashrrev_i32_e32 v113, 31, v112
	v_lshlrev_b64 v[112:113], 11, v[112:113]
	v_lshl_add_u64 v[112:113], v[112:113], 0, v[130:131]
	v_lshlrev_b64 v[120:121], 1, v[112:113]
	v_lshl_add_u64 v[116:117], s[46:47], 0, v[120:121]
	s_nop 0
	s_waitcnt vmcnt(10)
	v_mov_b64_e32 v[112:113], v[152:153]
	v_mov_b64_e32 v[114:115], v[154:155]
	v_mov_b64_e32 v[116:117], v[156:157]
	v_mov_b64_e32 v[118:119], v[158:159]
	global_load_dwordx4 v[144:147], v[246:247], off offset:16
	global_load_dwordx4 v[148:151], v[246:247], off
	global_load_dwordx4 v[152:155], v[248:249], off offset:16
	global_load_dwordx4 v[156:159], v[248:249], off
	v_lshlrev_b32_e32 v122, 16, v116
	v_and_b32_e32 v123, 0xffff0000, v116
	v_lshlrev_b32_e32 v116, 16, v117
	v_and_b32_e32 v117, 0xffff0000, v117
	v_pk_fma_f32 v[108:109], v[122:123], s[70:71], v[108:109] op_sel_hi:[1,0,1]
	v_pk_fma_f32 v[110:111], v[116:117], s[70:71], v[110:111] op_sel_hi:[1,0,1]
	v_cvt_pk_bf16_f32 v108, v108, v109
	v_cvt_pk_bf16_f32 v109, v110, v111
	v_lshlrev_b32_e32 v110, 16, v118
	v_and_b32_e32 v111, 0xffff0000, v118
	v_pk_fma_f32 v[104:105], v[110:111], s[70:71], v[104:105] op_sel_hi:[1,0,1]
	s_nop 0
	v_cvt_pk_bf16_f32 v110, v104, v105
	v_lshlrev_b32_e32 v104, 16, v119
	v_and_b32_e32 v105, 0xffff0000, v119
	v_pk_fma_f32 v[104:105], v[104:105], s[70:71], v[106:107] op_sel_hi:[1,0,1]
	s_nop 0
	v_cvt_pk_bf16_f32 v111, v104, v105
	v_lshlrev_b32_e32 v104, 16, v112
	v_and_b32_e32 v105, 0xffff0000, v112
	v_pk_fma_f32 v[100:101], v[104:105], s[70:71], v[100:101] op_sel_hi:[1,0,1]
	v_lshlrev_b32_e32 v104, 16, v113
	v_and_b32_e32 v105, 0xffff0000, v113
	v_pk_fma_f32 v[102:103], v[104:105], s[70:71], v[102:103] op_sel_hi:[1,0,1]
	v_cvt_pk_bf16_f32 v100, v100, v101
	v_cvt_pk_bf16_f32 v101, v102, v103
	v_lshlrev_b32_e32 v102, 16, v114
	v_and_b32_e32 v103, 0xffff0000, v114
	v_pk_fma_f32 v[96:97], v[102:103], s[70:71], v[96:97] op_sel_hi:[1,0,1]
	s_nop 0
	v_cvt_pk_bf16_f32 v102, v96, v97
	v_lshlrev_b32_e32 v96, 16, v115
	v_and_b32_e32 v97, 0xffff0000, v115
	v_pk_fma_f32 v[96:97], v[96:97], s[70:71], v[98:99] op_sel_hi:[1,0,1]
	s_nop 0
	v_cvt_pk_bf16_f32 v103, v96, v97
	v_lshl_add_u64 v[96:97], s[44:45], 0, v[120:121]
	global_store_dwordx4 v[96:97], v[108:111], off
	global_store_dwordx4 v[96:97], v[100:103], off offset:16
	v_or_b32_e32 v96, 32, v132
	v_ashrrev_i32_e32 v97, 31, v96
	v_lshlrev_b64 v[96:97], 11, v[96:97]
	v_lshl_add_u64 v[96:97], v[96:97], 0, v[130:131]
	v_lshlrev_b64 v[104:105], 1, v[96:97]
	v_lshl_add_u64 v[100:101], s[46:47], 0, v[104:105]
	s_nop 0
	s_waitcnt vmcnt(14)
; __device__ __forceinline__ unsigned cvt_pk_bf16(float lo, float hi) { typedef __bf16 bf16x2_t __attribute__((ext_vector_type(2))); f32x2 v = {lo, hi}; bf16x2_t b = __builtin_convertvector(v, bf16x2_t); return __builtin_bit_cast(unsigned, b); }
;     __device__ __forceinline__ void operator()(const f32x4 (&acc)[2][2][4][2], const Unit& u, int wr, int wc, int fr, int fq) const {
;     ...
;             for (int m = 0; m < 4; ++m) { const size_t off = (size_t)(row0 + ai * HALF + m * 16) * ldc + col0;
;                 const u32x4 ra = *(const u32x4*)(R + off), rb = *(const u32x4*)(R + off + 8);
;                 const f32x4 v0 = acc[ai][0][m][0], v1 = acc[ai][0][m][1], v2 = acc[ai][1][m][0], v3 = acc[ai][1][m][1];
;                 u32x4 wa, wb;
;                 wa.x = cvt_pk_bf16(bflo(ra.x) * alpha + v0[0], bfhi(ra.x) * alpha + v0[1]); wa.y = cvt_pk_bf16(bflo(ra.y) * alpha + v0[2], bfhi(ra.y) * alpha + v0[3]);
;                 wa.z = cvt_pk_bf16(bflo(ra.z) * alpha + v1[0], bfhi(ra.z) * alpha + v1[1]); wa.w = cvt_pk_bf16(bflo(ra.w) * alpha + v1[2], bfhi(ra.w) * alpha + v1[3]);
;                 wb.x = cvt_pk_bf16(bflo(rb.x) * alpha + v2[0], bfhi(rb.x) * alpha + v2[1]); wb.y = cvt_pk_bf16(bflo(rb.y) * alpha + v2[2], bfhi(rb.y) * alpha + v2[3]);
;                 wb.z = cvt_pk_bf16(bflo(rb.z) * alpha + v3[0], bfhi(rb.z) * alpha + v3[1]); wb.w = cvt_pk_bf16(bflo(rb.w) * alpha + v3[2], bfhi(rb.w) * alpha + v3[3]);
;                 *(u32x4*)(O + off) = wa; *(u32x4*)(O + off + 8) = wb; }
	v_mov_b64_e32 v[96:97], v[160:161]
	v_mov_b64_e32 v[98:99], v[162:163]
	v_mov_b64_e32 v[100:101], v[164:165]
	v_mov_b64_e32 v[102:103], v[166:167]
	v_lshlrev_b32_e32 v106, 16, v100
	v_and_b32_e32 v107, 0xffff0000, v100
	v_lshlrev_b32_e32 v100, 16, v101
	v_and_b32_e32 v101, 0xffff0000, v101
	v_pk_fma_f32 v[92:93], v[106:107], s[70:71], v[92:93] op_sel_hi:[1,0,1]
	v_pk_fma_f32 v[94:95], v[100:101], s[70:71], v[94:95] op_sel_hi:[1,0,1]
	v_cvt_pk_bf16_f32 v92, v92, v93
	v_cvt_pk_bf16_f32 v93, v94, v95
	v_lshlrev_b32_e32 v94, 16, v102
	v_and_b32_e32 v95, 0xffff0000, v102
	v_pk_fma_f32 v[88:89], v[94:95], s[70:71], v[88:89] op_sel_hi:[1,0,1]
	s_nop 0
	v_cvt_pk_bf16_f32 v94, v88, v89
	v_lshlrev_b32_e32 v88, 16, v103
	v_and_b32_e32 v89, 0xffff0000, v103
	v_pk_fma_f32 v[88:89], v[88:89], s[70:71], v[90:91] op_sel_hi:[1,0,1]
	s_nop 0
	v_cvt_pk_bf16_f32 v95, v88, v89
	v_lshlrev_b32_e32 v88, 16, v96
	v_and_b32_e32 v89, 0xffff0000, v96
	v_pk_fma_f32 v[84:85], v[88:89], s[70:71], v[84:85] op_sel_hi:[1,0,1]
	v_lshlrev_b32_e32 v88, 16, v97
	v_and_b32_e32 v89, 0xffff0000, v97
	v_pk_fma_f32 v[86:87], v[88:89], s[70:71], v[86:87] op_sel_hi:[1,0,1]
	v_cvt_pk_bf16_f32 v84, v84, v85
	v_cvt_pk_bf16_f32 v85, v86, v87
	v_lshlrev_b32_e32 v86, 16, v98
	v_and_b32_e32 v87, 0xffff0000, v98
	v_pk_fma_f32 v[80:81], v[86:87], s[70:71], v[80:81] op_sel_hi:[1,0,1]
	s_nop 0
	v_cvt_pk_bf16_f32 v86, v80, v81
	v_lshlrev_b32_e32 v80, 16, v99
	v_and_b32_e32 v81, 0xffff0000, v99
	v_pk_fma_f32 v[80:81], v[80:81], s[70:71], v[82:83] op_sel_hi:[1,0,1]
	s_nop 0
	v_cvt_pk_bf16_f32 v87, v80, v81
	v_lshl_add_u64 v[80:81], s[44:45], 0, v[104:105]
	global_store_dwordx4 v[80:81], v[92:95], off
	global_store_dwordx4 v[80:81], v[84:87], off offset:16
	v_or_b32_e32 v80, 48, v132
	v_ashrrev_i32_e32 v81, 31, v80
	v_lshlrev_b64 v[80:81], 11, v[80:81]
	v_lshl_add_u64 v[80:81], v[80:81], 0, v[130:131]
	v_lshlrev_b64 v[88:89], 1, v[80:81]
	v_lshl_add_u64 v[84:85], s[46:47], 0, v[88:89]
	s_nop 0
	s_waitcnt vmcnt(14)
	v_mov_b64_e32 v[80:81], v[168:169]
	v_mov_b64_e32 v[82:83], v[170:171]
	v_mov_b64_e32 v[84:85], v[172:173]
	v_mov_b64_e32 v[86:87], v[174:175]
	v_lshlrev_b32_e32 v90, 16, v84
	v_and_b32_e32 v91, 0xffff0000, v84
	v_lshlrev_b32_e32 v84, 16, v85
	v_and_b32_e32 v85, 0xffff0000, v85
	v_pk_fma_f32 v[76:77], v[90:91], s[70:71], v[76:77] op_sel_hi:[1,0,1]
	v_pk_fma_f32 v[78:79], v[84:85], s[70:71], v[78:79] op_sel_hi:[1,0,1]
	v_cvt_pk_bf16_f32 v76, v76, v77
	v_cvt_pk_bf16_f32 v77, v78, v79
	v_lshlrev_b32_e32 v78, 16, v86
	v_and_b32_e32 v79, 0xffff0000, v86
	v_pk_fma_f32 v[72:73], v[78:79], s[70:71], v[72:73] op_sel_hi:[1,0,1]
	s_nop 0
	v_cvt_pk_bf16_f32 v78, v72, v73
	v_lshlrev_b32_e32 v72, 16, v87
	v_and_b32_e32 v73, 0xffff0000, v87
	v_pk_fma_f32 v[72:73], v[72:73], s[70:71], v[74:75] op_sel_hi:[1,0,1]
	s_nop 0
	v_cvt_pk_bf16_f32 v79, v72, v73
	v_lshlrev_b32_e32 v72, 16, v80
	v_and_b32_e32 v73, 0xffff0000, v80
	v_pk_fma_f32 v[68:69], v[72:73], s[70:71], v[68:69] op_sel_hi:[1,0,1]
	v_lshlrev_b32_e32 v72, 16, v81
	v_and_b32_e32 v73, 0xffff0000, v81
	v_pk_fma_f32 v[70:71], v[72:73], s[70:71], v[70:71] op_sel_hi:[1,0,1]
	v_cvt_pk_bf16_f32 v68, v68, v69
	v_cvt_pk_bf16_f32 v69, v70, v71
	v_lshlrev_b32_e32 v70, 16, v82
	v_and_b32_e32 v71, 0xffff0000, v82
	v_pk_fma_f32 v[64:65], v[70:71], s[70:71], v[64:65] op_sel_hi:[1,0,1]
	v_lshl_add_u64 v[72:73], v[128:129], 0, s[8:9]
	v_cvt_pk_bf16_f32 v70, v64, v65
	v_lshlrev_b32_e32 v64, 16, v83
	v_and_b32_e32 v65, 0xffff0000, v83
	v_pk_fma_f32 v[64:65], v[64:65], s[70:71], v[66:67] op_sel_hi:[1,0,1]
	s_mov_b64 s[8:9], 0xa0000
	v_cvt_pk_bf16_f32 v71, v64, v65
	v_lshl_add_u64 v[64:65], s[44:45], 0, v[88:89]
	global_store_dwordx4 v[64:65], v[76:79], off
	global_store_dwordx4 v[64:65], v[68:71], off offset:16
	s_nop 1
	v_lshl_add_u64 v[68:69], s[46:47], 0, v[72:73]
	s_nop 0
	s_waitcnt vmcnt(14)
	v_mov_b64_e32 v[64:65], v[176:177]
	v_mov_b64_e32 v[66:67], v[178:179]
	v_mov_b64_e32 v[68:69], v[180:181]
	v_mov_b64_e32 v[70:71], v[182:183]
	v_lshlrev_b32_e32 v74, 16, v68
	v_and_b32_e32 v75, 0xffff0000, v68
	v_lshlrev_b32_e32 v68, 16, v69
	v_and_b32_e32 v69, 0xffff0000, v69
	v_pk_fma_f32 v[60:61], v[74:75], s[70:71], v[60:61] op_sel_hi:[1,0,1]
	v_pk_fma_f32 v[62:63], v[68:69], s[70:71], v[62:63] op_sel_hi:[1,0,1]
	v_cvt_pk_bf16_f32 v60, v60, v61
	v_cvt_pk_bf16_f32 v61, v62, v63
	v_lshlrev_b32_e32 v62, 16, v70
	v_and_b32_e32 v63, 0xffff0000, v70
	v_pk_fma_f32 v[56:57], v[62:63], s[70:71], v[56:57] op_sel_hi:[1,0,1]
	s_nop 0
	v_cvt_pk_bf16_f32 v62, v56, v57
	v_lshlrev_b32_e32 v56, 16, v71
	v_and_b32_e32 v57, 0xffff0000, v71
	v_pk_fma_f32 v[56:57], v[56:57], s[70:71], v[58:59] op_sel_hi:[1,0,1]
	s_nop 0
	v_cvt_pk_bf16_f32 v63, v56, v57
	v_lshlrev_b32_e32 v56, 16, v64
	v_and_b32_e32 v57, 0xffff0000, v64
	v_pk_fma_f32 v[52:53], v[56:57], s[70:71], v[52:53] op_sel_hi:[1,0,1]
	v_lshlrev_b32_e32 v56, 16, v65
	v_and_b32_e32 v57, 0xffff0000, v65
	v_pk_fma_f32 v[54:55], v[56:57], s[70:71], v[54:55] op_sel_hi:[1,0,1]
	v_cvt_pk_bf16_f32 v52, v52, v53
	v_cvt_pk_bf16_f32 v53, v54, v55
	v_lshlrev_b32_e32 v54, 16, v66
	v_and_b32_e32 v55, 0xffff0000, v66
	v_pk_fma_f32 v[48:49], v[54:55], s[70:71], v[48:49] op_sel_hi:[1,0,1]
	v_lshl_add_u64 v[56:57], v[128:129], 0, s[68:69]
	v_cvt_pk_bf16_f32 v54, v48, v49
	v_lshlrev_b32_e32 v48, 16, v67
	v_and_b32_e32 v49, 0xffff0000, v67
	v_pk_fma_f32 v[48:49], v[48:49], s[70:71], v[50:51] op_sel_hi:[1,0,1]
	s_nop 0
	v_cvt_pk_bf16_f32 v55, v48, v49
	v_lshl_add_u64 v[48:49], s[44:45], 0, v[72:73]
	global_store_dwordx4 v[48:49], v[60:63], off
	global_store_dwordx4 v[48:49], v[52:55], off offset:16
	s_nop 1
	v_lshl_add_u64 v[52:53], s[46:47], 0, v[56:57]
	s_nop 0
	s_waitcnt vmcnt(14)
; __device__ __forceinline__ unsigned cvt_pk_bf16(float lo, float hi) { typedef __bf16 bf16x2_t __attribute__((ext_vector_type(2))); f32x2 v = {lo, hi}; bf16x2_t b = __builtin_convertvector(v, bf16x2_t); return __builtin_bit_cast(unsigned, b); }
;     __device__ __forceinline__ void operator()(const f32x4 (&acc)[2][2][4][2], const Unit& u, int wr, int wc, int fr, int fq) const {
;     ...
;             for (int m = 0; m < 4; ++m) { const size_t off = (size_t)(row0 + ai * HALF + m * 16) * ldc + col0;
;                 const u32x4 ra = *(const u32x4*)(R + off), rb = *(const u32x4*)(R + off + 8);
;                 const f32x4 v0 = acc[ai][0][m][0], v1 = acc[ai][0][m][1], v2 = acc[ai][1][m][0], v3 = acc[ai][1][m][1];
;                 u32x4 wa, wb;
;                 wa.x = cvt_pk_bf16(bflo(ra.x) * alpha + v0[0], bfhi(ra.x) * alpha + v0[1]); wa.y = cvt_pk_bf16(bflo(ra.y) * alpha + v0[2], bfhi(ra.y) * alpha + v0[3]);
;                 wa.z = cvt_pk_bf16(bflo(ra.z) * alpha + v1[0], bfhi(ra.z) * alpha + v1[1]); wa.w = cvt_pk_bf16(bflo(ra.w) * alpha + v1[2], bfhi(ra.w) * alpha + v1[3]);
;                 wb.x = cvt_pk_bf16(bflo(rb.x) * alpha + v2[0], bfhi(rb.x) * alpha + v2[1]); wb.y = cvt_pk_bf16(bflo(rb.y) * alpha + v2[2], bfhi(rb.y) * alpha + v2[3]);
;                 wb.z = cvt_pk_bf16(bflo(rb.z) * alpha + v3[0], bfhi(rb.z) * alpha + v3[1]); wb.w = cvt_pk_bf16(bflo(rb.w) * alpha + v3[2], bfhi(rb.w) * alpha + v3[3]);
;                 *(u32x4*)(O + off) = wa; *(u32x4*)(O + off + 8) = wb; }
	v_mov_b64_e32 v[48:49], v[184:185]
	v_mov_b64_e32 v[50:51], v[186:187]
	v_mov_b64_e32 v[52:53], v[188:189]
	v_mov_b64_e32 v[54:55], v[190:191]
	v_lshlrev_b32_e32 v58, 16, v52
	v_and_b32_e32 v59, 0xffff0000, v52
	v_lshlrev_b32_e32 v52, 16, v53
	v_and_b32_e32 v53, 0xffff0000, v53
	v_pk_fma_f32 v[44:45], v[58:59], s[70:71], v[44:45] op_sel_hi:[1,0,1]
	v_pk_fma_f32 v[46:47], v[52:53], s[70:71], v[46:47] op_sel_hi:[1,0,1]
	v_cvt_pk_bf16_f32 v44, v44, v45
	v_cvt_pk_bf16_f32 v45, v46, v47
	v_lshlrev_b32_e32 v46, 16, v54
	v_and_b32_e32 v47, 0xffff0000, v54
	v_pk_fma_f32 v[40:41], v[46:47], s[70:71], v[40:41] op_sel_hi:[1,0,1]
	s_nop 0
	v_cvt_pk_bf16_f32 v46, v40, v41
	v_lshlrev_b32_e32 v40, 16, v55
	v_and_b32_e32 v41, 0xffff0000, v55
	v_pk_fma_f32 v[40:41], v[40:41], s[70:71], v[42:43] op_sel_hi:[1,0,1]
	s_nop 0
	v_cvt_pk_bf16_f32 v47, v40, v41
	v_lshlrev_b32_e32 v40, 16, v48
	v_and_b32_e32 v41, 0xffff0000, v48
	v_pk_fma_f32 v[36:37], v[40:41], s[70:71], v[36:37] op_sel_hi:[1,0,1]
	v_lshlrev_b32_e32 v40, 16, v49
	v_and_b32_e32 v41, 0xffff0000, v49
	v_pk_fma_f32 v[38:39], v[40:41], s[70:71], v[38:39] op_sel_hi:[1,0,1]
	v_cvt_pk_bf16_f32 v36, v36, v37
	v_cvt_pk_bf16_f32 v37, v38, v39
	v_lshlrev_b32_e32 v38, 16, v50
	v_and_b32_e32 v39, 0xffff0000, v50
	v_pk_fma_f32 v[32:33], v[38:39], s[70:71], v[32:33] op_sel_hi:[1,0,1]
	v_lshl_add_u64 v[40:41], v[128:129], 0, s[8:9]
	v_cvt_pk_bf16_f32 v38, v32, v33
	v_lshlrev_b32_e32 v32, 16, v51
	v_and_b32_e32 v33, 0xffff0000, v51
	v_pk_fma_f32 v[32:33], v[32:33], s[70:71], v[34:35] op_sel_hi:[1,0,1]
	s_mov_b64 s[8:9], 0xb0000
	v_cvt_pk_bf16_f32 v39, v32, v33
	v_lshl_add_u64 v[32:33], s[44:45], 0, v[56:57]
	global_store_dwordx4 v[32:33], v[44:47], off
	global_store_dwordx4 v[32:33], v[36:39], off offset:16
	s_nop 1
	v_lshl_add_u64 v[36:37], s[46:47], 0, v[40:41]
	s_nop 0
	s_waitcnt vmcnt(12)
	v_mov_b64_e32 v[32:33], v[144:145]
	v_mov_b64_e32 v[34:35], v[146:147]
	v_mov_b64_e32 v[36:37], v[148:149]
	v_mov_b64_e32 v[38:39], v[150:151]
	v_lshlrev_b32_e32 v42, 16, v36
	v_and_b32_e32 v43, 0xffff0000, v36
	v_lshlrev_b32_e32 v36, 16, v37
	v_and_b32_e32 v37, 0xffff0000, v37
	v_pk_fma_f32 v[28:29], v[42:43], s[70:71], v[28:29] op_sel_hi:[1,0,1]
	v_pk_fma_f32 v[30:31], v[36:37], s[70:71], v[30:31] op_sel_hi:[1,0,1]
	v_cvt_pk_bf16_f32 v28, v28, v29
	v_cvt_pk_bf16_f32 v29, v30, v31
	v_lshlrev_b32_e32 v30, 16, v38
	v_and_b32_e32 v31, 0xffff0000, v38
	v_pk_fma_f32 v[24:25], v[30:31], s[70:71], v[24:25] op_sel_hi:[1,0,1]
	s_nop 0
	v_cvt_pk_bf16_f32 v30, v24, v25
	v_lshlrev_b32_e32 v24, 16, v39
	v_and_b32_e32 v25, 0xffff0000, v39
	v_pk_fma_f32 v[24:25], v[24:25], s[70:71], v[26:27] op_sel_hi:[1,0,1]
	s_nop 0
	v_cvt_pk_bf16_f32 v31, v24, v25
	v_lshlrev_b32_e32 v24, 16, v32
	v_and_b32_e32 v25, 0xffff0000, v32
	v_pk_fma_f32 v[20:21], v[24:25], s[70:71], v[20:21] op_sel_hi:[1,0,1]
	v_lshlrev_b32_e32 v24, 16, v33
	v_and_b32_e32 v25, 0xffff0000, v33
	v_pk_fma_f32 v[22:23], v[24:25], s[70:71], v[22:23] op_sel_hi:[1,0,1]
	v_cvt_pk_bf16_f32 v20, v20, v21
	v_cvt_pk_bf16_f32 v21, v22, v23
	v_lshlrev_b32_e32 v22, 16, v34
	v_and_b32_e32 v23, 0xffff0000, v34
	v_pk_fma_f32 v[16:17], v[22:23], s[70:71], v[16:17] op_sel_hi:[1,0,1]
	v_lshl_add_u64 v[24:25], v[128:129], 0, s[8:9]
	v_cvt_pk_bf16_f32 v22, v16, v17
	v_lshlrev_b32_e32 v16, 16, v35
	v_and_b32_e32 v17, 0xffff0000, v35
	v_pk_fma_f32 v[16:17], v[16:17], s[70:71], v[18:19] op_sel_hi:[1,0,1]
	s_mov_b64 s[8:9], -1
	v_cvt_pk_bf16_f32 v23, v16, v17
	v_lshl_add_u64 v[16:17], s[44:45], 0, v[40:41]
	global_store_dwordx4 v[16:17], v[28:31], off
	global_store_dwordx4 v[16:17], v[20:23], off offset:16
	s_nop 1
	v_lshl_add_u64 v[20:21], s[46:47], 0, v[24:25]
	s_nop 0
	s_waitcnt vmcnt(12)
	v_mov_b64_e32 v[16:17], v[152:153]
	v_mov_b64_e32 v[18:19], v[154:155]
	v_mov_b64_e32 v[20:21], v[156:157]
	v_mov_b64_e32 v[22:23], v[158:159]
	v_lshlrev_b32_e32 v26, 16, v20
	v_and_b32_e32 v27, 0xffff0000, v20
	v_lshlrev_b32_e32 v20, 16, v21
	v_and_b32_e32 v21, 0xffff0000, v21
	v_pk_fma_f32 v[12:13], v[26:27], s[70:71], v[12:13] op_sel_hi:[1,0,1]
	v_pk_fma_f32 v[14:15], v[20:21], s[70:71], v[14:15] op_sel_hi:[1,0,1]
	v_cvt_pk_bf16_f32 v12, v12, v13
	v_cvt_pk_bf16_f32 v13, v14, v15
	v_lshlrev_b32_e32 v14, 16, v22
	v_and_b32_e32 v15, 0xffff0000, v22
	v_pk_fma_f32 v[8:9], v[14:15], s[70:71], v[8:9] op_sel_hi:[1,0,1]
	s_nop 0
	v_cvt_pk_bf16_f32 v14, v8, v9
	v_lshlrev_b32_e32 v8, 16, v23
	v_and_b32_e32 v9, 0xffff0000, v23
	v_pk_fma_f32 v[8:9], v[8:9], s[70:71], v[10:11] op_sel_hi:[1,0,1]
	s_nop 0
	v_cvt_pk_bf16_f32 v15, v8, v9
	v_lshlrev_b32_e32 v8, 16, v16
	v_and_b32_e32 v9, 0xffff0000, v16
	v_pk_fma_f32 v[4:5], v[8:9], s[70:71], v[4:5] op_sel_hi:[1,0,1]
	v_lshlrev_b32_e32 v8, 16, v17
	v_and_b32_e32 v9, 0xffff0000, v17
	v_pk_fma_f32 v[6:7], v[8:9], s[70:71], v[6:7] op_sel_hi:[1,0,1]
	v_cvt_pk_bf16_f32 v4, v4, v5
	v_cvt_pk_bf16_f32 v5, v6, v7
	v_lshlrev_b32_e32 v6, 16, v18
	v_and_b32_e32 v7, 0xffff0000, v18
	v_pk_fma_f32 v[0:1], v[6:7], s[70:71], v[0:1] op_sel_hi:[1,0,1]
	s_nop 0
	v_cvt_pk_bf16_f32 v6, v0, v1
	v_lshlrev_b32_e32 v0, 16, v19
	v_and_b32_e32 v1, 0xffff0000, v19
	v_pk_fma_f32 v[0:1], v[0:1], s[70:71], v[2:3] op_sel_hi:[1,0,1]
	s_nop 0
	v_cvt_pk_bf16_f32 v7, v0, v1
	v_lshl_add_u64 v[0:1], s[44:45], 0, v[24:25]
	global_store_dwordx4 v[0:1], v[12:15], off
	global_store_dwordx4 v[0:1], v[4:7], off offset:16
	s_cbranch_vccnz .LBB0_718
	s_andn2_b64 vcc, exec, s[42:43]
	s_cbranch_vccnz .LBB0_717
	s_barrier
	s_branch .LBB0_717

; __device__ __forceinline__ void ln_router_tile(const Frame& F, const bf16* yf, const float* g1, const float* b1, bf16* x1b, bf16* x1l, unsigned char* x1q, const bf16* __restrict__ rthi, const bf16* __restrict__ rtlo, ...
;     ...
;     for (int rq = 0; rq < 8; rq += 4) {
;     u32x2 yraw[4][8];
; #pragma unroll
;     for (int r4 = 0; r4 < 4; ++r4) { const u32x2* yr = (const u32x2*)(yf + (size_t)(t0 + 8 * w + rq + r4) * D) + lane;
; #pragma unroll
;         for (int j = 0; j < 8; ++j) yraw[r4][j] = __builtin_nontemporal_load(yr + 64 * j); }
; #pragma unroll
;     for (int r4 = 0; r4 < 4; ++r4) {
;         const int t = t0 + 8 * w + rq + r4;
;         f32x4 v[8]; float s = 0.f;
; #pragma unroll
;         for (int j = 0; j < 8; ++j) { const u32x2 y = yraw[r4][j]; v[j] = (f32x4){bflo(y.x), bfhi(y.x), bflo(y.y), bfhi(y.y)}; s += (v[j].x + v[j].y) + (v[j].z + v[j].w); }
.LBB0_790:
	s_waitcnt vmcnt(0)
	v_mov_b32_e32 v0, v193
	s_lshl_b32 s96, s79, 6
	v_mbcnt_lo_u32_b32 v0, -1, v0
	v_mbcnt_hi_u32_b32 v0, -1, v0
	v_add_u32_e32 v16, s31, v0
	v_mov_b32_e32 v19, v193
	v_and_b32_e32 v20, 63, v16
	v_lshlrev_b32_e32 v24, 4, v20
	v_lshlrev_b32_e32 v192, 3, v20
	v_lshlrev_b32_e32 v18, 2, v20
	v_mov_b32_e32 v25, v193
	v_or_b32_e32 v8, 0x1000, v24
	v_mov_b32_e32 v9, v193
	v_or_b32_e32 v12, 0x1400, v24
	v_mov_b32_e32 v13, v193
	v_or_b32_e32 v22, 0x1800, v24
	v_mov_b32_e32 v23, v193
	v_or_b32_e32 v26, 0x1c00, v24
	v_mov_b32_e32 v27, v193
	s_mov_b32 s6, 0
	s_add_i32 s97, s96, s34
	v_lshl_add_u64 v[0:1], s[44:45], 0, v[192:193]
	v_lshl_add_u64 v[2:3], s[90:91], 0, v[24:25]
	v_lshl_add_u64 v[4:5], s[92:93], 0, v[24:25]
	v_lshl_add_u64 v[6:7], s[90:91], 0, v[8:9]
	v_lshl_add_u64 v[8:9], s[92:93], 0, v[8:9]
	v_lshl_add_u64 v[10:11], s[90:91], 0, v[12:13]
	v_lshl_add_u64 v[12:13], s[92:93], 0, v[12:13]
	v_lshl_add_u64 v[14:15], s[90:91], 0, v[22:23]
	v_lshl_add_u64 v[22:23], s[92:93], 0, v[22:23]
	v_lshl_add_u64 v[24:25], s[90:91], 0, v[26:27]
	v_lshl_add_u64 v[26:27], s[92:93], 0, v[26:27]
	v_lshl_add_u64 v[28:29], s[46:47], 0, v[192:193]
	v_lshl_add_u64 v[30:31], s[48:49], 0, v[192:193]
	v_lshl_add_u64 v[32:33], s[50:51], 0, v[18:19]
	s_mov_b64 s[4:5], -1
	global_load_dwordx4 v[128:131], v[2:3], off
	global_load_dwordx4 v[132:135], v[2:3], off offset:1024
	global_load_dwordx4 v[136:139], v[2:3], off offset:2048
	global_load_dwordx4 v[140:143], v[2:3], off offset:3072
	global_load_dwordx4 v[144:147], v[6:7], off
	global_load_dwordx4 v[148:151], v[10:11], off
	global_load_dwordx4 v[152:155], v[14:15], off
	global_load_dwordx4 v[156:159], v[24:25], off
	global_load_dwordx4 v[160:163], v[4:5], off
	global_load_dwordx4 v[164:167], v[4:5], off offset:1024
	global_load_dwordx4 v[168:171], v[4:5], off offset:2048
	global_load_dwordx4 v[172:175], v[4:5], off offset:3072
	global_load_dwordx4 v[176:179], v[8:9], off
	global_load_dwordx4 v[180:183], v[12:13], off
	global_load_dwordx4 v[184:187], v[22:23], off
	global_load_dwordx4 v[188:191], v[26:27], off
.LBB0_791:
	s_or_b32 s6, s6, s97
	s_ashr_i32 s7, s6, 31
	s_lshl_b64 s[12:13], s[6:7], 12
	v_lshl_add_u64 v[34:35], v[0:1], 0, s[12:13]
	global_load_dwordx2 v[82:83], v[34:35], off nt
	global_load_dwordx2 v[84:85], v[34:35], off offset:512 nt
	global_load_dwordx2 v[86:87], v[34:35], off offset:1024 nt
	global_load_dwordx2 v[88:89], v[34:35], off offset:1536 nt
	global_load_dwordx2 v[90:91], v[34:35], off offset:2048 nt
	global_load_dwordx2 v[92:93], v[34:35], off offset:2560 nt
	global_load_dwordx2 v[94:95], v[34:35], off offset:3072 nt
	global_load_dwordx2 v[96:97], v[34:35], off offset:3584 nt
	v_cndmask_b32_e64 v17, 0, 1, s[4:5]
	v_cmp_ne_u32_e32 vcc, 1, v17
	s_or_b32 s10, s6, 1
	s_ashr_i32 s11, s10, 31
	s_or_b32 s36, s6, 2
	s_or_b32 s42, s6, 3
	s_lshl_b64 s[8:9], s[10:11], 12
	s_ashr_i32 s37, s36, 31
	s_ashr_i32 s43, s42, 31
	s_lshl_b64 s[4:5], s[36:37], 12
	s_lshl_b64 s[38:39], s[42:43], 12
	v_lshl_add_u64 v[34:35], v[0:1], 0, s[8:9]
	global_load_dwordx2 v[80:81], v[34:35], off nt
	global_load_dwordx2 v[78:79], v[34:35], off offset:512 nt
	global_load_dwordx2 v[76:77], v[34:35], off offset:1024 nt
	global_load_dwordx2 v[74:75], v[34:35], off offset:1536 nt
	global_load_dwordx2 v[72:73], v[34:35], off offset:2048 nt
	global_load_dwordx2 v[70:71], v[34:35], off offset:2560 nt
	global_load_dwordx2 v[68:69], v[34:35], off offset:3072 nt
	global_load_dwordx2 v[66:67], v[34:35], off offset:3584 nt
	v_lshl_add_u64 v[34:35], v[0:1], 0, s[4:5]
	v_lshl_add_u64 v[36:37], v[0:1], 0, s[38:39]
	global_load_dwordx2 v[64:65], v[34:35], off nt
	global_load_dwordx2 v[62:63], v[34:35], off offset:512 nt
	global_load_dwordx2 v[60:61], v[34:35], off offset:1024 nt
	global_load_dwordx2 v[58:59], v[34:35], off offset:1536 nt
	global_load_dwordx2 v[56:57], v[34:35], off offset:2048 nt
	global_load_dwordx2 v[54:55], v[34:35], off offset:2560 nt
	global_load_dwordx2 v[52:53], v[34:35], off offset:3072 nt
	global_load_dwordx2 v[50:51], v[34:35], off offset:3584 nt
	global_load_dwordx2 v[48:49], v[36:37], off nt
	global_load_dwordx2 v[46:47], v[36:37], off offset:512 nt
	global_load_dwordx2 v[44:45], v[36:37], off offset:1024 nt
	global_load_dwordx2 v[42:43], v[36:37], off offset:1536 nt
	global_load_dwordx2 v[40:41], v[36:37], off offset:2048 nt
	global_load_dwordx2 v[38:39], v[36:37], off offset:2560 nt
	global_load_dwordx2 v[34:35], v[36:37], off offset:3072 nt
	s_nop 0
	global_load_dwordx2 v[36:37], v[36:37], off offset:3584 nt
	s_lshl_b64 s[14:15], s[6:7], 11
	s_lshl_b64 s[6:7], s[36:37], 11
	s_lshl_b64 s[10:11], s[10:11], 11
	s_lshl_b64 s[42:43], s[42:43], 11
	s_and_b64 vcc, exec, vcc
	s_waitcnt vmcnt(31)
	v_lshlrev_b32_e32 v118, 16, v82
	v_and_b32_e32 v119, 0xffff0000, v82
	v_lshlrev_b32_e32 v124, 16, v83
	v_and_b32_e32 v125, 0xffff0000, v83
	v_add_f32_e32 v17, v118, v119
	v_add_f32_e32 v19, v124, v125
	s_waitcnt vmcnt(30)
	v_lshlrev_b32_e32 v114, 16, v84
	v_and_b32_e32 v115, 0xffff0000, v84
	v_lshlrev_b32_e32 v116, 16, v85
	v_and_b32_e32 v117, 0xffff0000, v85
	v_add_f32_e32 v17, v17, v19
	v_add_f32_e32 v19, v114, v115
	v_add_f32_e32 v21, v116, v117
	v_add_f32_e32 v17, 0, v17
	v_add_f32_e32 v19, v19, v21
	s_waitcnt vmcnt(29)
	v_lshlrev_b32_e32 v110, 16, v86
	v_and_b32_e32 v111, 0xffff0000, v86
	v_lshlrev_b32_e32 v112, 16, v87
	v_and_b32_e32 v113, 0xffff0000, v87
	v_add_f32_e32 v17, v17, v19
	v_add_f32_e32 v19, v110, v111
	v_add_f32_e32 v21, v112, v113
	v_add_f32_e32 v19, v19, v21
	s_waitcnt vmcnt(28)
; __device__ __forceinline__ void ln_router_tile(const Frame& F, const bf16* yf, const float* g1, const float* b1, bf16* x1b, bf16* x1l, unsigned char* x1q, const bf16* __restrict__ rthi, const bf16* __restrict__ rtlo, ...
;     ...
; #pragma unroll
;         for (int j = 0; j < 8; ++j) { const u32x2 y = yraw[r4][j]; v[j] = (f32x4){bflo(y.x), bfhi(y.x), bflo(y.y), bfhi(y.y)}; s += (v[j].x + v[j].y) + (v[j].z + v[j].w); }
;         const float mean = wave_sum(s) * (1.0f / D); float s2 = 0.f;
; #pragma unroll
;         for (int j = 0; j < 8; ++j) { v[j] = v[j] - mean; s2 += (v[j].x * v[j].x + v[j].y * v[j].y) + (v[j].z * v[j].z + v[j].w * v[j].w); }
;         const float rstd = rsqrtf(wave_sum(s2) * (1.0f / D) + EPS);
; #pragma unroll
;         for (int j = 0; j < 8; ++j) { const int c = 4 * lane + 256 * j; const f32x4 gg = *(const f32x4*)(g1 + c), bb = *(const f32x4*)(b1 + c);
;             const f32x4 o = v[j] * rstd * gg + bb;
	v_lshlrev_b32_e32 v106, 16, v88
	v_and_b32_e32 v107, 0xffff0000, v88
	v_lshlrev_b32_e32 v108, 16, v89
	v_and_b32_e32 v109, 0xffff0000, v89
	v_add_f32_e32 v17, v17, v19
	v_add_f32_e32 v19, v106, v107
	v_add_f32_e32 v21, v108, v109
	v_add_f32_e32 v19, v19, v21
	s_waitcnt vmcnt(27)
	v_lshlrev_b32_e32 v102, 16, v90
	v_and_b32_e32 v103, 0xffff0000, v90
	v_lshlrev_b32_e32 v104, 16, v91
	v_and_b32_e32 v105, 0xffff0000, v91
	v_add_f32_e32 v17, v17, v19
	v_add_f32_e32 v19, v102, v103
	v_add_f32_e32 v21, v104, v105
	v_add_f32_e32 v19, v19, v21
	s_waitcnt vmcnt(26)
	v_lshlrev_b32_e32 v98, 16, v92
	v_and_b32_e32 v99, 0xffff0000, v92
	v_lshlrev_b32_e32 v100, 16, v93
	v_and_b32_e32 v101, 0xffff0000, v93
	v_add_f32_e32 v17, v17, v19
	v_add_f32_e32 v19, v98, v99
	v_add_f32_e32 v21, v100, v101
	v_add_f32_e32 v19, v19, v21
	s_waitcnt vmcnt(25)
	v_lshlrev_b32_e32 v90, 16, v94
	v_and_b32_e32 v91, 0xffff0000, v94
	v_lshlrev_b32_e32 v92, 16, v95
	v_and_b32_e32 v93, 0xffff0000, v95
	v_add_f32_e32 v17, v17, v19
	v_add_f32_e32 v19, v90, v91
	v_add_f32_e32 v21, v92, v93
	v_add_f32_e32 v19, v19, v21
	s_waitcnt vmcnt(24)
	v_lshlrev_b32_e32 v82, 16, v96
	v_and_b32_e32 v83, 0xffff0000, v96
	v_lshlrev_b32_e32 v84, 16, v97
	v_and_b32_e32 v85, 0xffff0000, v97
	v_add_f32_e32 v17, v17, v19
	v_add_f32_e32 v19, v82, v83
	v_add_f32_e32 v21, v84, v85
	v_add_f32_e32 v19, v19, v21
	v_add_f32_e32 v17, v17, v19
	s_nop 1
	v_add_f32_dpp v17, v17, v17 quad_perm:[1,0,3,2] row_mask:0xf bank_mask:0xf bound_ctrl:1
	s_nop 1
	v_add_f32_dpp v17, v17, v17 quad_perm:[2,3,0,1] row_mask:0xf bank_mask:0xf bound_ctrl:1
	s_nop 1
	v_add_f32_dpp v17, v17, v17 row_half_mirror row_mask:0xf bank_mask:0xf bound_ctrl:1
	s_nop 1
	v_add_f32_dpp v17, v17, v17 row_mirror row_mask:0xf bank_mask:0xf bound_ctrl:1
	v_mov_b32_e32 v19, v17
	s_nop 1
	v_permlane32_swap_b32 v19, v17
	s_nop 0
	v_add_f32_e32 v17, v19, v17
	s_nop 0
	v_readlane_b32 s37, v17, 16
	v_readlane_b32 s36, v17, 0
	s_nop 0
	v_mov_b32_e32 v17, s37
	v_add_f32_e32 v17, s36, v17
	v_fmac_f32_e32 v125, 0xba000000, v17
	v_fmac_f32_e32 v119, 0xba000000, v17
	v_fmac_f32_e32 v124, 0xba000000, v17
	v_fmac_f32_e32 v118, 0xba000000, v17
	v_mul_f32_e32 v19, v119, v119
	v_mul_f32_e32 v21, v125, v125
	v_fmac_f32_e32 v19, v118, v118
	v_fmac_f32_e32 v21, v124, v124
	v_fmac_f32_e32 v117, 0xba000000, v17
	v_fmac_f32_e32 v115, 0xba000000, v17
	v_add_f32_e32 v19, v19, v21
	v_fmac_f32_e32 v116, 0xba000000, v17
	v_fmac_f32_e32 v114, 0xba000000, v17
	v_mul_f32_e32 v21, v115, v115
	v_mul_f32_e32 v86, v117, v117
	v_fmac_f32_e32 v21, v114, v114
	v_fmac_f32_e32 v86, v116, v116
	v_add_f32_e32 v21, v21, v86
	v_fmac_f32_e32 v113, 0xba000000, v17
	v_fmac_f32_e32 v111, 0xba000000, v17
	v_add_f32_e32 v19, v19, v21
	v_fmac_f32_e32 v112, 0xba000000, v17
	v_fmac_f32_e32 v110, 0xba000000, v17
	v_mul_f32_e32 v21, v111, v111
	v_mul_f32_e32 v86, v113, v113
	v_fmac_f32_e32 v21, v110, v110
	v_fmac_f32_e32 v86, v112, v112
	v_add_f32_e32 v21, v21, v86
	v_fmac_f32_e32 v109, 0xba000000, v17
	v_fmac_f32_e32 v107, 0xba000000, v17
	v_add_f32_e32 v19, v21, v19
	v_fmac_f32_e32 v108, 0xba000000, v17
	v_fmac_f32_e32 v106, 0xba000000, v17
	v_mul_f32_e32 v21, v107, v107
	v_mul_f32_e32 v86, v109, v109
	v_fmac_f32_e32 v21, v106, v106
	v_fmac_f32_e32 v86, v108, v108
	v_add_f32_e32 v21, v21, v86
	v_fmac_f32_e32 v105, 0xba000000, v17
	v_fmac_f32_e32 v103, 0xba000000, v17
	v_add_f32_e32 v19, v21, v19
	v_fmac_f32_e32 v104, 0xba000000, v17
	v_fmac_f32_e32 v102, 0xba000000, v17
	v_mul_f32_e32 v21, v103, v103
	v_mul_f32_e32 v86, v105, v105
	v_fmac_f32_e32 v21, v102, v102
	v_fmac_f32_e32 v86, v104, v104
	v_add_f32_e32 v21, v21, v86
	v_fmac_f32_e32 v101, 0xba000000, v17
	v_fmac_f32_e32 v99, 0xba000000, v17
	v_add_f32_e32 v19, v21, v19
	v_fmac_f32_e32 v100, 0xba000000, v17
	v_fmac_f32_e32 v98, 0xba000000, v17
	v_mul_f32_e32 v21, v99, v99
	v_mul_f32_e32 v86, v101, v101
	v_fmac_f32_e32 v21, v98, v98
	v_fmac_f32_e32 v86, v100, v100
	v_add_f32_e32 v21, v21, v86
	v_fmac_f32_e32 v93, 0xba000000, v17
	v_fmac_f32_e32 v91, 0xba000000, v17
	v_add_f32_e32 v19, v21, v19
	v_fmac_f32_e32 v92, 0xba000000, v17
	v_fmac_f32_e32 v90, 0xba000000, v17
	v_mul_f32_e32 v21, v91, v91
	v_mul_f32_e32 v86, v93, v93
	v_fmac_f32_e32 v21, v90, v90
	v_fmac_f32_e32 v86, v92, v92
	v_add_f32_e32 v21, v21, v86
	v_fmac_f32_e32 v85, 0xba000000, v17
	v_fmac_f32_e32 v83, 0xba000000, v17
	v_add_f32_e32 v19, v21, v19
	v_fmac_f32_e32 v84, 0xba000000, v17
	v_fmac_f32_e32 v82, 0xba000000, v17
	v_mul_f32_e32 v17, v83, v83
	v_mul_f32_e32 v21, v85, v85
	v_fmac_f32_e32 v17, v82, v82
	v_fmac_f32_e32 v21, v84, v84
	v_add_f32_e32 v17, v17, v21
	v_add_f32_e32 v17, v17, v19
	s_nop 1
	v_add_f32_dpp v17, v17, v17 quad_perm:[1,0,3,2] row_mask:0xf bank_mask:0xf bound_ctrl:1
	s_nop 1
	v_add_f32_dpp v17, v17, v17 quad_perm:[2,3,0,1] row_mask:0xf bank_mask:0xf bound_ctrl:1
	s_nop 1
	v_add_f32_dpp v17, v17, v17 row_half_mirror row_mask:0xf bank_mask:0xf bound_ctrl:1
	s_nop 1
	v_add_f32_dpp v17, v17, v17 row_mirror row_mask:0xf bank_mask:0xf bound_ctrl:1
	v_mov_b32_e32 v19, v17
	s_nop 1
	v_permlane32_swap_b32 v17, v19
	v_mov_b64_e32 v[94:95], v[128:129]
	v_mov_b64_e32 v[96:97], v[130:131]
	v_mov_b64_e32 v[120:121], v[160:161]
	v_mov_b64_e32 v[122:123], v[162:163]
	v_add_f32_e32 v17, v17, v19
	s_nop 0
	v_readlane_b32 s37, v17, 16
	v_readlane_b32 s36, v17, 0
	s_nop 0
	v_mov_b32_e32 v17, s37
	v_add_f32_e32 v17, s36, v17
	v_fmamk_f32 v17, v17, 0x3a000000, v194
	v_cmp_gt_f32_e64 s[36:37], s26, v17
	v_mul_f32_e32 v19, 0x4b800000, v17
	s_nop 0
	v_cndmask_b32_e64 v17, v17, v19, s[36:37]
	v_rsq_f32_e32 v17, v17
	s_nop 0
	v_mul_f32_e32 v19, 0x45800000, v17
	v_cndmask_b32_e64 v88, v17, v19, s[36:37]
	v_pk_mul_f32 v[86:87], v[118:119], v[88:89] op_sel_hi:[1,0]
	v_mov_b32_e32 v17, v193
	v_pk_mul_f32 v[118:119], v[124:125], v[88:89] op_sel_hi:[1,0]
	v_pk_mul_f32 v[114:115], v[114:115], v[88:89] op_sel_hi:[1,0]
	v_pk_mul_f32 v[116:117], v[116:117], v[88:89] op_sel_hi:[1,0]
	v_pk_mul_f32 v[110:111], v[110:111], v[88:89] op_sel_hi:[1,0]
	v_pk_mul_f32 v[112:113], v[112:113], v[88:89] op_sel_hi:[1,0]
	v_pk_mul_f32 v[106:107], v[106:107], v[88:89] op_sel_hi:[1,0]
	v_pk_mul_f32 v[108:109], v[108:109], v[88:89] op_sel_hi:[1,0]
	v_pk_mul_f32 v[102:103], v[102:103], v[88:89] op_sel_hi:[1,0]
	v_pk_mul_f32 v[104:105], v[104:105], v[88:89] op_sel_hi:[1,0]
	v_pk_mul_f32 v[98:99], v[98:99], v[88:89] op_sel_hi:[1,0]
	v_pk_mul_f32 v[100:101], v[100:101], v[88:89] op_sel_hi:[1,0]
	v_pk_mul_f32 v[90:91], v[90:91], v[88:89] op_sel_hi:[1,0]
	v_pk_mul_f32 v[92:93], v[92:93], v[88:89] op_sel_hi:[1,0]
	v_pk_mul_f32 v[82:83], v[82:83], v[88:89] op_sel_hi:[1,0]
	v_pk_mul_f32 v[84:85], v[84:85], v[88:89] op_sel_hi:[1,0]
	s_waitcnt vmcnt(0)
; __device__ __forceinline__ unsigned pk2(float lo, float hi) { return hw_pk_bf16(lo, hi); }
; __device__ __forceinline__ unsigned pk4_fp8(float a, float b, float c, float d) { int w = __builtin_amdgcn_cvt_pk_fp8_f32(a, b, 0, false); w = __builtin_amdgcn_cvt_pk_fp8_f32(c, d, w, true); return (unsigned)w; }
; __device__ __forceinline__ void ln_router_tile(const Frame& F, const bf16* yf, const float* g1, const float* b1, bf16* x1b, bf16* x1l, unsigned char* x1q, const bf16* __restrict__ rthi, const bf16* __restrict__ rtlo, ...
;     ...
; #pragma unroll
;         for (int j = 0; j < 8; ++j) { const int c = 4 * lane + 256 * j; const f32x4 gg = *(const f32x4*)(g1 + c), bb = *(const f32x4*)(b1 + c);
;             const f32x4 o = v[j] * rstd * gg + bb;
;             u32x2 wh; wh.x = pk2(o.x, o.y); wh.y = pk2(o.z, o.w); *(u32x2*)(x1b + (size_t)t * D + c) = wh;
;             u32x2 wl; wl.x = pk2(o.x - bflo(wh.x), o.y - bfhi(wh.x)); wl.y = pk2(o.z - bflo(wh.y), o.w - bfhi(wh.y)); *(u32x2*)(x1l + (size_t)t * D + c) = wl;
;             if (x1q) *(unsigned*)(x1q + (size_t)t * D + c) = pk4_fp8(o.x, o.y, o.z, o.w); }
	v_pk_fma_f32 v[120:121], v[94:95], v[86:87], v[120:121]
	s_nop 0
	v_cvt_pk_fp8_f32 v17, v120, v121
	v_cvt_pk_bf16_f32 v86, v120, v121
	v_pk_fma_f32 v[118:119], v[96:97], v[118:119], v[122:123]
	v_lshlrev_b32_e32 v96, 16, v86
	v_and_b32_e32 v97, 0xffff0000, v86
	v_cvt_pk_bf16_f32 v87, v118, v119
	v_lshl_add_u64 v[94:95], v[28:29], 0, s[12:13]
	v_pk_add_f32 v[96:97], v[120:121], v[96:97] neg_lo:[0,1] neg_hi:[0,1]
	global_store_dwordx2 v[94:95], v[86:87], off
	v_cvt_pk_bf16_f32 v86, v96, v97
	v_lshlrev_b32_e32 v96, 16, v87
	v_and_b32_e32 v97, 0xffff0000, v87
	v_cvt_pk_fp8_f32 v17, v118, v119 op_sel:[0,0,1]
	v_pk_add_f32 v[96:97], v[118:119], v[96:97] neg_lo:[0,1] neg_hi:[0,1]
	s_nop 0
	v_cvt_pk_bf16_f32 v87, v96, v97
	v_lshl_add_u64 v[96:97], v[30:31], 0, s[12:13]
	global_store_dwordx2 v[96:97], v[86:87], off
	v_lshl_add_u64 v[86:87], v[32:33], 0, s[14:15]
	global_store_dword v[86:87], v17, off
	v_mov_b64_e32 v[118:119], v[132:133]
	v_mov_b64_e32 v[120:121], v[134:135]
	v_mov_b64_e32 v[122:123], v[164:165]
	v_mov_b64_e32 v[124:125], v[166:167]
	v_mov_b32_e32 v17, v193
	v_pk_fma_f32 v[114:115], v[118:119], v[114:115], v[122:123]
	s_nop 0
	v_cvt_pk_fp8_f32 v17, v114, v115
	v_cvt_pk_bf16_f32 v118, v114, v115
	v_pk_fma_f32 v[116:117], v[120:121], v[116:117], v[124:125]
	v_lshlrev_b32_e32 v120, 16, v118
	v_and_b32_e32 v121, 0xffff0000, v118
	v_cvt_pk_bf16_f32 v119, v116, v117
	v_pk_add_f32 v[120:121], v[114:115], v[120:121] neg_lo:[0,1] neg_hi:[0,1]
	v_cvt_pk_fp8_f32 v17, v116, v117 op_sel:[0,0,1]
	global_store_dwordx2 v[94:95], v[118:119], off offset:512
	v_cvt_pk_bf16_f32 v118, v120, v121
	v_lshlrev_b32_e32 v120, 16, v119
	v_and_b32_e32 v121, 0xffff0000, v119
	v_pk_add_f32 v[120:121], v[116:117], v[120:121] neg_lo:[0,1] neg_hi:[0,1]
	s_nop 0
	v_cvt_pk_bf16_f32 v119, v120, v121
	global_store_dwordx2 v[96:97], v[118:119], off offset:512
	global_store_dword v[86:87], v17, off offset:256
	v_mov_b64_e32 v[114:115], v[136:137]
	v_mov_b64_e32 v[116:117], v[138:139]
	s_nop 0
	v_mov_b64_e32 v[118:119], v[168:169]
	v_mov_b64_e32 v[120:121], v[170:171]
	v_mov_b32_e32 v17, v193
	v_pk_fma_f32 v[110:111], v[110:111], v[114:115], v[118:119]
	s_nop 0
	v_cvt_pk_fp8_f32 v17, v110, v111
	v_cvt_pk_bf16_f32 v114, v110, v111
	v_pk_fma_f32 v[112:113], v[112:113], v[116:117], v[120:121]
	v_lshlrev_b32_e32 v116, 16, v114
	v_and_b32_e32 v117, 0xffff0000, v114
	v_cvt_pk_bf16_f32 v115, v112, v113
	v_pk_add_f32 v[116:117], v[110:111], v[116:117] neg_lo:[0,1] neg_hi:[0,1]
	v_cvt_pk_fp8_f32 v17, v112, v113 op_sel:[0,0,1]
	global_store_dwordx2 v[94:95], v[114:115], off offset:1024
	v_cvt_pk_bf16_f32 v114, v116, v117
	v_lshlrev_b32_e32 v116, 16, v115
	v_and_b32_e32 v117, 0xffff0000, v115
	v_pk_add_f32 v[116:117], v[112:113], v[116:117] neg_lo:[0,1] neg_hi:[0,1]
	s_nop 0
	v_cvt_pk_bf16_f32 v115, v116, v117
	global_store_dwordx2 v[96:97], v[114:115], off offset:1024
	global_store_dword v[86:87], v17, off offset:512
	v_mov_b64_e32 v[110:111], v[140:141]
	v_mov_b64_e32 v[112:113], v[142:143]
	s_nop 0
	v_mov_b64_e32 v[114:115], v[172:173]
	v_mov_b64_e32 v[116:117], v[174:175]
	v_mov_b32_e32 v17, v193
	v_pk_fma_f32 v[106:107], v[106:107], v[110:111], v[114:115]
	s_nop 0
	v_cvt_pk_fp8_f32 v17, v106, v107
	v_cvt_pk_bf16_f32 v110, v106, v107
	v_pk_fma_f32 v[108:109], v[108:109], v[112:113], v[116:117]
	v_lshlrev_b32_e32 v112, 16, v110
	v_and_b32_e32 v113, 0xffff0000, v110
	v_cvt_pk_bf16_f32 v111, v108, v109
	v_pk_add_f32 v[112:113], v[106:107], v[112:113] neg_lo:[0,1] neg_hi:[0,1]
	v_cvt_pk_fp8_f32 v17, v108, v109 op_sel:[0,0,1]
	global_store_dwordx2 v[94:95], v[110:111], off offset:1536
	v_cvt_pk_bf16_f32 v110, v112, v113
	v_lshlrev_b32_e32 v112, 16, v111
	v_and_b32_e32 v113, 0xffff0000, v111
	v_pk_add_f32 v[112:113], v[108:109], v[112:113] neg_lo:[0,1] neg_hi:[0,1]
	s_nop 0
	v_cvt_pk_bf16_f32 v111, v112, v113
	global_store_dwordx2 v[96:97], v[110:111], off offset:1536
	global_store_dword v[86:87], v17, off offset:768
	v_mov_b64_e32 v[106:107], v[144:145]
	v_mov_b64_e32 v[108:109], v[146:147]
	s_nop 0
	v_mov_b64_e32 v[110:111], v[176:177]
	v_mov_b64_e32 v[112:113], v[178:179]
	v_mov_b32_e32 v17, v193
	v_pk_fma_f32 v[102:103], v[102:103], v[106:107], v[110:111]
	s_nop 0
	v_cvt_pk_fp8_f32 v17, v102, v103
	v_cvt_pk_bf16_f32 v106, v102, v103
	v_pk_fma_f32 v[104:105], v[104:105], v[108:109], v[112:113]
	v_lshlrev_b32_e32 v108, 16, v106
	v_and_b32_e32 v109, 0xffff0000, v106
	v_cvt_pk_bf16_f32 v107, v104, v105
	v_pk_add_f32 v[108:109], v[102:103], v[108:109] neg_lo:[0,1] neg_hi:[0,1]
	v_cvt_pk_fp8_f32 v17, v104, v105 op_sel:[0,0,1]
	global_store_dwordx2 v[94:95], v[106:107], off offset:2048
	v_cvt_pk_bf16_f32 v106, v108, v109
	v_lshlrev_b32_e32 v108, 16, v107
	v_and_b32_e32 v109, 0xffff0000, v107
	v_pk_add_f32 v[108:109], v[104:105], v[108:109] neg_lo:[0,1] neg_hi:[0,1]
	s_nop 0
	v_cvt_pk_bf16_f32 v107, v108, v109
	global_store_dwordx2 v[96:97], v[106:107], off offset:2048
	global_store_dword v[86:87], v17, off offset:1024
	v_mov_b64_e32 v[102:103], v[148:149]
	v_mov_b64_e32 v[104:105], v[150:151]
	s_nop 0
	v_mov_b64_e32 v[106:107], v[180:181]
	v_mov_b64_e32 v[108:109], v[182:183]
	v_mov_b32_e32 v17, v193
	v_pk_fma_f32 v[98:99], v[98:99], v[102:103], v[106:107]
	s_nop 0
	v_cvt_pk_fp8_f32 v17, v98, v99
	v_cvt_pk_bf16_f32 v102, v98, v99
	v_pk_fma_f32 v[100:101], v[100:101], v[104:105], v[108:109]
	v_lshlrev_b32_e32 v104, 16, v102
	v_and_b32_e32 v105, 0xffff0000, v102
	v_cvt_pk_bf16_f32 v103, v100, v101
	v_pk_add_f32 v[104:105], v[98:99], v[104:105] neg_lo:[0,1] neg_hi:[0,1]
	v_cvt_pk_fp8_f32 v17, v100, v101 op_sel:[0,0,1]
	global_store_dwordx2 v[94:95], v[102:103], off offset:2560
; __device__ __forceinline__ unsigned pk2(float lo, float hi) { return hw_pk_bf16(lo, hi); }
; __device__ __forceinline__ unsigned pk4_fp8(float a, float b, float c, float d) { int w = __builtin_amdgcn_cvt_pk_fp8_f32(a, b, 0, false); w = __builtin_amdgcn_cvt_pk_fp8_f32(c, d, w, true); return (unsigned)w; }
; __device__ __forceinline__ void ln_router_tile(const Frame& F, const bf16* yf, const float* g1, const float* b1, bf16* x1b, bf16* x1l, unsigned char* x1q, const bf16* __restrict__ rthi, const bf16* __restrict__ rtlo, ...
;     ...
; #pragma unroll
;         for (int j = 0; j < 8; ++j) { const u32x2 y = yraw[r4][j]; v[j] = (f32x4){bflo(y.x), bfhi(y.x), bflo(y.y), bfhi(y.y)}; s += (v[j].x + v[j].y) + (v[j].z + v[j].w); }
;         const float mean = wave_sum(s) * (1.0f / D); float s2 = 0.f;
; #pragma unroll
;         for (int j = 0; j < 8; ++j) { v[j] = v[j] - mean; s2 += (v[j].x * v[j].x + v[j].y * v[j].y) + (v[j].z * v[j].z + v[j].w * v[j].w); }
;     ...
; #pragma unroll
;         for (int j = 0; j < 8; ++j) { const int c = 4 * lane + 256 * j; const f32x4 gg = *(const f32x4*)(g1 + c), bb = *(const f32x4*)(b1 + c);
;             const f32x4 o = v[j] * rstd * gg + bb;
;             u32x2 wh; wh.x = pk2(o.x, o.y); wh.y = pk2(o.z, o.w); *(u32x2*)(x1b + (size_t)t * D + c) = wh;
;             u32x2 wl; wl.x = pk2(o.x - bflo(wh.x), o.y - bfhi(wh.x)); wl.y = pk2(o.z - bflo(wh.y), o.w - bfhi(wh.y)); *(u32x2*)(x1l + (size_t)t * D + c) = wl;
;             if (x1q) *(unsigned*)(x1q + (size_t)t * D + c) = pk4_fp8(o.x, o.y, o.z, o.w); }
	v_cvt_pk_bf16_f32 v102, v104, v105
	v_lshlrev_b32_e32 v104, 16, v103
	v_and_b32_e32 v105, 0xffff0000, v103
	v_pk_add_f32 v[104:105], v[100:101], v[104:105] neg_lo:[0,1] neg_hi:[0,1]
	v_lshlrev_b32_e32 v108, 16, v81
	v_cvt_pk_bf16_f32 v103, v104, v105
	global_store_dwordx2 v[96:97], v[102:103], off offset:2560
	global_store_dword v[86:87], v17, off offset:1280
	v_mov_b64_e32 v[98:99], v[152:153]
	v_mov_b64_e32 v[100:101], v[154:155]
	s_nop 0
	v_mov_b64_e32 v[102:103], v[184:185]
	v_mov_b64_e32 v[104:105], v[186:187]
	v_mov_b32_e32 v17, v193
	v_and_b32_e32 v109, 0xffff0000, v81
	v_add_f32_e32 v19, v108, v109
	v_pk_fma_f32 v[90:91], v[90:91], v[98:99], v[102:103]
	s_nop 0
	v_cvt_pk_fp8_f32 v17, v90, v91
	v_cvt_pk_bf16_f32 v98, v90, v91
	v_pk_fma_f32 v[92:93], v[92:93], v[100:101], v[104:105]
	v_lshlrev_b32_e32 v100, 16, v98
	v_and_b32_e32 v101, 0xffff0000, v98
	v_cvt_pk_bf16_f32 v99, v92, v93
	v_pk_add_f32 v[100:101], v[90:91], v[100:101] neg_lo:[0,1] neg_hi:[0,1]
	v_cvt_pk_fp8_f32 v17, v92, v93 op_sel:[0,0,1]
	global_store_dwordx2 v[94:95], v[98:99], off offset:3072
	v_cvt_pk_bf16_f32 v98, v100, v101
	v_lshlrev_b32_e32 v100, 16, v99
	v_and_b32_e32 v101, 0xffff0000, v99
	v_pk_add_f32 v[100:101], v[92:93], v[100:101] neg_lo:[0,1] neg_hi:[0,1]
	v_lshlrev_b32_e32 v102, 16, v80
	v_cvt_pk_bf16_f32 v99, v100, v101
	global_store_dwordx2 v[96:97], v[98:99], off offset:3072
	global_store_dword v[86:87], v17, off offset:1536
	v_mov_b64_e32 v[90:91], v[156:157]
	v_mov_b64_e32 v[92:93], v[158:159]
	s_nop 0
	v_mov_b64_e32 v[98:99], v[188:189]
	v_mov_b64_e32 v[100:101], v[190:191]
	v_mov_b32_e32 v17, v193
	v_and_b32_e32 v103, 0xffff0000, v80
	v_pk_fma_f32 v[82:83], v[82:83], v[90:91], v[98:99]
	s_nop 0
	v_cvt_pk_fp8_f32 v17, v82, v83
	v_cvt_pk_bf16_f32 v88, v82, v83
	v_pk_fma_f32 v[84:85], v[84:85], v[92:93], v[100:101]
	v_lshlrev_b32_e32 v90, 16, v88
	v_and_b32_e32 v91, 0xffff0000, v88
	v_cvt_pk_bf16_f32 v89, v84, v85
	v_pk_add_f32 v[90:91], v[82:83], v[90:91] neg_lo:[0,1] neg_hi:[0,1]
	v_cvt_pk_fp8_f32 v17, v84, v85 op_sel:[0,0,1]
	global_store_dwordx2 v[94:95], v[88:89], off offset:3584
	v_cvt_pk_bf16_f32 v88, v90, v91
	v_lshlrev_b32_e32 v90, 16, v89
	v_and_b32_e32 v91, 0xffff0000, v89
	v_pk_add_f32 v[90:91], v[84:85], v[90:91] neg_lo:[0,1] neg_hi:[0,1]
	v_lshlrev_b32_e32 v98, 16, v78
	v_cvt_pk_bf16_f32 v89, v90, v91
	global_store_dwordx2 v[96:97], v[88:89], off offset:3584
	global_store_dword v[86:87], v17, off offset:1792
	v_add_f32_e32 v17, v102, v103
	v_and_b32_e32 v99, 0xffff0000, v78
	v_lshlrev_b32_e32 v100, 16, v79
	v_and_b32_e32 v101, 0xffff0000, v79
	v_add_f32_e32 v17, v17, v19
	v_add_f32_e32 v19, v98, v99
	v_add_f32_e32 v21, v100, v101
	v_add_f32_e32 v17, 0, v17
	v_add_f32_e32 v19, v19, v21
	v_lshlrev_b32_e32 v94, 16, v76
	v_and_b32_e32 v95, 0xffff0000, v76
	v_lshlrev_b32_e32 v96, 16, v77
	v_and_b32_e32 v97, 0xffff0000, v77
	v_add_f32_e32 v17, v17, v19
	v_add_f32_e32 v19, v94, v95
	v_add_f32_e32 v21, v96, v97
	v_add_f32_e32 v19, v19, v21
	v_lshlrev_b32_e32 v90, 16, v74
	v_and_b32_e32 v91, 0xffff0000, v74
	v_lshlrev_b32_e32 v92, 16, v75
	v_and_b32_e32 v93, 0xffff0000, v75
	v_add_f32_e32 v17, v17, v19
	v_add_f32_e32 v19, v90, v91
	v_add_f32_e32 v21, v92, v93
	v_add_f32_e32 v19, v19, v21
	v_lshlrev_b32_e32 v86, 16, v72
	v_and_b32_e32 v87, 0xffff0000, v72
	v_lshlrev_b32_e32 v88, 16, v73
	v_and_b32_e32 v89, 0xffff0000, v73
	v_add_f32_e32 v17, v17, v19
	v_add_f32_e32 v19, v86, v87
	v_add_f32_e32 v21, v88, v89
	v_add_f32_e32 v19, v19, v21
	v_lshlrev_b32_e32 v82, 16, v70
	v_and_b32_e32 v83, 0xffff0000, v70
	v_lshlrev_b32_e32 v84, 16, v71
	v_and_b32_e32 v85, 0xffff0000, v71
	v_add_f32_e32 v17, v17, v19
	v_add_f32_e32 v19, v82, v83
	v_add_f32_e32 v21, v84, v85
	v_add_f32_e32 v19, v19, v21
	v_lshlrev_b32_e32 v74, 16, v68
	v_and_b32_e32 v75, 0xffff0000, v68
	v_lshlrev_b32_e32 v76, 16, v69
	v_and_b32_e32 v77, 0xffff0000, v69
	v_add_f32_e32 v17, v17, v19
	v_add_f32_e32 v19, v74, v75
	v_add_f32_e32 v21, v76, v77
	v_add_f32_e32 v19, v19, v21
	v_lshlrev_b32_e32 v68, 16, v66
	v_and_b32_e32 v69, 0xffff0000, v66
	v_lshlrev_b32_e32 v66, 16, v67
	v_and_b32_e32 v67, 0xffff0000, v67
	v_add_f32_e32 v17, v17, v19
	v_add_f32_e32 v19, v68, v69
	v_add_f32_e32 v21, v66, v67
	v_add_f32_e32 v19, v19, v21
	v_add_f32_e32 v17, v17, v19
	s_nop 1
	v_add_f32_dpp v17, v17, v17 quad_perm:[1,0,3,2] row_mask:0xf bank_mask:0xf bound_ctrl:1
	s_nop 1
	v_add_f32_dpp v17, v17, v17 quad_perm:[2,3,0,1] row_mask:0xf bank_mask:0xf bound_ctrl:1
	s_nop 1
	v_add_f32_dpp v17, v17, v17 row_half_mirror row_mask:0xf bank_mask:0xf bound_ctrl:1
	s_nop 1
	v_add_f32_dpp v17, v17, v17 row_mirror row_mask:0xf bank_mask:0xf bound_ctrl:1
	v_mov_b32_e32 v19, v17
	s_nop 1
	v_permlane32_swap_b32 v19, v17
	s_nop 0
	v_add_f32_e32 v17, v19, v17
	s_nop 0
	v_readlane_b32 s13, v17, 16
	v_readlane_b32 s12, v17, 0
	s_nop 0
	v_mov_b32_e32 v17, s13
	v_add_f32_e32 v17, s12, v17
	v_fmac_f32_e32 v109, 0xba000000, v17
	v_fmac_f32_e32 v103, 0xba000000, v17
	v_fmac_f32_e32 v108, 0xba000000, v17
	v_fmac_f32_e32 v102, 0xba000000, v17
	v_mul_f32_e32 v19, v103, v103
	v_mul_f32_e32 v21, v109, v109
	v_fmac_f32_e32 v19, v102, v102
	v_fmac_f32_e32 v21, v108, v108
	v_fmac_f32_e32 v101, 0xba000000, v17
	v_fmac_f32_e32 v99, 0xba000000, v17
	v_add_f32_e32 v19, v19, v21
	v_fmac_f32_e32 v100, 0xba000000, v17
	v_fmac_f32_e32 v98, 0xba000000, v17
	v_mul_f32_e32 v21, v99, v99
	v_mul_f32_e32 v70, v101, v101
	v_fmac_f32_e32 v21, v98, v98
	v_fmac_f32_e32 v70, v100, v100
	v_add_f32_e32 v21, v21, v70
	v_fmac_f32_e32 v97, 0xba000000, v17
	v_fmac_f32_e32 v95, 0xba000000, v17
	v_add_f32_e32 v19, v19, v21
	v_fmac_f32_e32 v96, 0xba000000, v17
; __device__ __forceinline__ unsigned pk2(float lo, float hi) { return hw_pk_bf16(lo, hi); }
; __device__ __forceinline__ unsigned pk4_fp8(float a, float b, float c, float d) { int w = __builtin_amdgcn_cvt_pk_fp8_f32(a, b, 0, false); w = __builtin_amdgcn_cvt_pk_fp8_f32(c, d, w, true); return (unsigned)w; }
; __device__ __forceinline__ void ln_router_tile(const Frame& F, const bf16* yf, const float* g1, const float* b1, bf16* x1b, bf16* x1l, unsigned char* x1q, const bf16* __restrict__ rthi, const bf16* __restrict__ rtlo, ...
;     ...
;     for (int r4 = 0; r4 < 4; ++r4) {
;         const int t = t0 + 8 * w + rq + r4;
;         f32x4 v[8]; float s = 0.f;
; #pragma unroll
;         for (int j = 0; j < 8; ++j) { const u32x2 y = yraw[r4][j]; v[j] = (f32x4){bflo(y.x), bfhi(y.x), bflo(y.y), bfhi(y.y)}; s += (v[j].x + v[j].y) + (v[j].z + v[j].w); }
;         const float mean = wave_sum(s) * (1.0f / D); float s2 = 0.f;
; #pragma unroll
;         for (int j = 0; j < 8; ++j) { v[j] = v[j] - mean; s2 += (v[j].x * v[j].x + v[j].y * v[j].y) + (v[j].z * v[j].z + v[j].w * v[j].w); }
;         const float rstd = rsqrtf(wave_sum(s2) * (1.0f / D) + EPS);
; #pragma unroll
;         for (int j = 0; j < 8; ++j) { const int c = 4 * lane + 256 * j; const f32x4 gg = *(const f32x4*)(g1 + c), bb = *(const f32x4*)(b1 + c);
;             const f32x4 o = v[j] * rstd * gg + bb;
;             u32x2 wh; wh.x = pk2(o.x, o.y); wh.y = pk2(o.z, o.w); *(u32x2*)(x1b + (size_t)t * D + c) = wh;
;             u32x2 wl; wl.x = pk2(o.x - bflo(wh.x), o.y - bfhi(wh.x)); wl.y = pk2(o.z - bflo(wh.y), o.w - bfhi(wh.y)); *(u32x2*)(x1l + (size_t)t * D + c) = wl;
;             if (x1q) *(unsigned*)(x1q + (size_t)t * D + c) = pk4_fp8(o.x, o.y, o.z, o.w); }
	v_fmac_f32_e32 v94, 0xba000000, v17
	v_mul_f32_e32 v21, v95, v95
	v_mul_f32_e32 v70, v97, v97
	v_fmac_f32_e32 v21, v94, v94
	v_fmac_f32_e32 v70, v96, v96
	v_add_f32_e32 v21, v21, v70
	v_fmac_f32_e32 v93, 0xba000000, v17
	v_fmac_f32_e32 v91, 0xba000000, v17
	v_add_f32_e32 v19, v21, v19
	v_fmac_f32_e32 v92, 0xba000000, v17
	v_fmac_f32_e32 v90, 0xba000000, v17
	v_mul_f32_e32 v21, v91, v91
	v_mul_f32_e32 v70, v93, v93
	v_fmac_f32_e32 v21, v90, v90
	v_fmac_f32_e32 v70, v92, v92
	v_add_f32_e32 v21, v21, v70
	v_fmac_f32_e32 v89, 0xba000000, v17
	v_fmac_f32_e32 v87, 0xba000000, v17
	v_add_f32_e32 v19, v21, v19
	v_fmac_f32_e32 v88, 0xba000000, v17
	v_fmac_f32_e32 v86, 0xba000000, v17
	v_mul_f32_e32 v21, v87, v87
	v_mul_f32_e32 v70, v89, v89
	v_fmac_f32_e32 v21, v86, v86
	v_fmac_f32_e32 v70, v88, v88
	v_add_f32_e32 v21, v21, v70
	v_fmac_f32_e32 v85, 0xba000000, v17
	v_fmac_f32_e32 v83, 0xba000000, v17
	v_add_f32_e32 v19, v21, v19
	v_fmac_f32_e32 v84, 0xba000000, v17
	v_fmac_f32_e32 v82, 0xba000000, v17
	v_mul_f32_e32 v21, v83, v83
	v_mul_f32_e32 v70, v85, v85
	v_fmac_f32_e32 v21, v82, v82
	v_fmac_f32_e32 v70, v84, v84
	v_add_f32_e32 v21, v21, v70
	v_fmac_f32_e32 v77, 0xba000000, v17
	v_fmac_f32_e32 v75, 0xba000000, v17
	v_add_f32_e32 v19, v21, v19
	v_fmac_f32_e32 v76, 0xba000000, v17
	v_fmac_f32_e32 v74, 0xba000000, v17
	v_mul_f32_e32 v21, v75, v75
	v_mul_f32_e32 v70, v77, v77
	v_fmac_f32_e32 v21, v74, v74
	v_fmac_f32_e32 v70, v76, v76
	v_add_f32_e32 v21, v21, v70
	v_fmac_f32_e32 v67, 0xba000000, v17
	v_fmac_f32_e32 v69, 0xba000000, v17
	v_add_f32_e32 v19, v21, v19
	v_fmac_f32_e32 v66, 0xba000000, v17
	v_fmac_f32_e32 v68, 0xba000000, v17
	v_mul_f32_e32 v17, v69, v69
	v_mul_f32_e32 v21, v67, v67
	v_fmac_f32_e32 v17, v68, v68
	v_fmac_f32_e32 v21, v66, v66
	v_add_f32_e32 v17, v17, v21
	v_add_f32_e32 v17, v17, v19
	s_nop 1
	v_add_f32_dpp v17, v17, v17 quad_perm:[1,0,3,2] row_mask:0xf bank_mask:0xf bound_ctrl:1
	s_nop 1
	v_add_f32_dpp v17, v17, v17 quad_perm:[2,3,0,1] row_mask:0xf bank_mask:0xf bound_ctrl:1
	s_nop 1
	v_add_f32_dpp v17, v17, v17 row_half_mirror row_mask:0xf bank_mask:0xf bound_ctrl:1
	s_nop 1
	v_add_f32_dpp v17, v17, v17 row_mirror row_mask:0xf bank_mask:0xf bound_ctrl:1
	v_mov_b32_e32 v19, v17
	s_nop 1
	v_permlane32_swap_b32 v19, v17
	v_mov_b64_e32 v[78:79], v[128:129]
	v_mov_b64_e32 v[80:81], v[130:131]
	v_mov_b64_e32 v[104:105], v[160:161]
	v_mov_b64_e32 v[106:107], v[162:163]
	v_add_f32_e32 v17, v19, v17
	s_nop 0
	v_readlane_b32 s13, v17, 16
	v_readlane_b32 s12, v17, 0
	s_nop 0
	v_mov_b32_e32 v17, s13
	v_add_f32_e32 v17, s12, v17
	v_fmamk_f32 v17, v17, 0x3a000000, v194
	v_cmp_gt_f32_e64 s[36:37], s26, v17
	v_mul_f32_e32 v19, 0x4b800000, v17
	s_nop 0
	v_cndmask_b32_e64 v17, v17, v19, s[36:37]
	v_rsq_f32_e32 v17, v17
	s_nop 0
	v_mul_f32_e32 v19, 0x45800000, v17
	v_cndmask_b32_e64 v72, v17, v19, s[36:37]
	v_pk_mul_f32 v[70:71], v[102:103], v[72:73] op_sel_hi:[1,0]
	v_mov_b32_e32 v17, v193
	v_pk_mul_f32 v[102:103], v[108:109], v[72:73] op_sel_hi:[1,0]
	v_pk_mul_f32 v[98:99], v[98:99], v[72:73] op_sel_hi:[1,0]
	v_pk_mul_f32 v[100:101], v[100:101], v[72:73] op_sel_hi:[1,0]
	v_pk_mul_f32 v[94:95], v[94:95], v[72:73] op_sel_hi:[1,0]
	v_pk_mul_f32 v[96:97], v[96:97], v[72:73] op_sel_hi:[1,0]
	v_pk_mul_f32 v[90:91], v[90:91], v[72:73] op_sel_hi:[1,0]
	v_pk_mul_f32 v[92:93], v[92:93], v[72:73] op_sel_hi:[1,0]
	v_pk_mul_f32 v[86:87], v[86:87], v[72:73] op_sel_hi:[1,0]
	v_pk_mul_f32 v[88:89], v[88:89], v[72:73] op_sel_hi:[1,0]
	v_pk_mul_f32 v[82:83], v[82:83], v[72:73] op_sel_hi:[1,0]
	v_pk_mul_f32 v[84:85], v[84:85], v[72:73] op_sel_hi:[1,0]
	v_pk_mul_f32 v[74:75], v[74:75], v[72:73] op_sel_hi:[1,0]
	v_pk_mul_f32 v[76:77], v[76:77], v[72:73] op_sel_hi:[1,0]
	v_pk_mul_f32 v[68:69], v[68:69], v[72:73] op_sel_hi:[1,0]
	v_pk_mul_f32 v[66:67], v[66:67], v[72:73] op_sel_hi:[1,0]
	v_pk_fma_f32 v[104:105], v[78:79], v[70:71], v[104:105]
	s_nop 0
	v_cvt_pk_fp8_f32 v17, v104, v105
	v_cvt_pk_bf16_f32 v70, v104, v105
	v_pk_fma_f32 v[102:103], v[80:81], v[102:103], v[106:107]
	v_lshlrev_b32_e32 v80, 16, v70
	v_and_b32_e32 v81, 0xffff0000, v70
	v_cvt_pk_bf16_f32 v71, v102, v103
	v_lshl_add_u64 v[78:79], v[28:29], 0, s[8:9]
	v_pk_add_f32 v[80:81], v[104:105], v[80:81] neg_lo:[0,1] neg_hi:[0,1]
	global_store_dwordx2 v[78:79], v[70:71], off
	v_cvt_pk_bf16_f32 v70, v80, v81
	v_lshlrev_b32_e32 v80, 16, v71
	v_and_b32_e32 v81, 0xffff0000, v71
	v_cvt_pk_fp8_f32 v17, v102, v103 op_sel:[0,0,1]
	v_pk_add_f32 v[80:81], v[102:103], v[80:81] neg_lo:[0,1] neg_hi:[0,1]
	s_nop 0
	v_cvt_pk_bf16_f32 v71, v80, v81
	v_lshl_add_u64 v[80:81], v[30:31], 0, s[8:9]
	global_store_dwordx2 v[80:81], v[70:71], off
	v_lshl_add_u64 v[70:71], v[32:33], 0, s[10:11]
	global_store_dword v[70:71], v17, off
	v_mov_b64_e32 v[102:103], v[132:133]
	v_mov_b64_e32 v[104:105], v[134:135]
	v_mov_b64_e32 v[106:107], v[164:165]
	v_mov_b64_e32 v[108:109], v[166:167]
	v_mov_b32_e32 v17, v193
	v_pk_fma_f32 v[98:99], v[102:103], v[98:99], v[106:107]
	s_nop 0
	v_cvt_pk_fp8_f32 v17, v98, v99
	v_cvt_pk_bf16_f32 v102, v98, v99
	v_pk_fma_f32 v[100:101], v[104:105], v[100:101], v[108:109]
	v_lshlrev_b32_e32 v104, 16, v102
	v_and_b32_e32 v105, 0xffff0000, v102
	v_cvt_pk_bf16_f32 v103, v100, v101
	v_pk_add_f32 v[104:105], v[98:99], v[104:105] neg_lo:[0,1] neg_hi:[0,1]
	v_cvt_pk_fp8_f32 v17, v100, v101 op_sel:[0,0,1]
	global_store_dwordx2 v[78:79], v[102:103], off offset:512
	v_cvt_pk_bf16_f32 v102, v104, v105
	v_lshlrev_b32_e32 v104, 16, v103
	v_and_b32_e32 v105, 0xffff0000, v103
	v_pk_add_f32 v[104:105], v[100:101], v[104:105] neg_lo:[0,1] neg_hi:[0,1]
	s_nop 0
	v_cvt_pk_bf16_f32 v103, v104, v105
; __device__ __forceinline__ unsigned pk2(float lo, float hi) { return hw_pk_bf16(lo, hi); }
; __device__ __forceinline__ unsigned pk4_fp8(float a, float b, float c, float d) { int w = __builtin_amdgcn_cvt_pk_fp8_f32(a, b, 0, false); w = __builtin_amdgcn_cvt_pk_fp8_f32(c, d, w, true); return (unsigned)w; }
; __device__ __forceinline__ void ln_router_tile(const Frame& F, const bf16* yf, const float* g1, const float* b1, bf16* x1b, bf16* x1l, unsigned char* x1q, const bf16* __restrict__ rthi, const bf16* __restrict__ rtlo, ...
;     ...
;         for (int j = 0; j < 8; ++j) { const u32x2 y = yraw[r4][j]; v[j] = (f32x4){bflo(y.x), bfhi(y.x), bflo(y.y), bfhi(y.y)}; s += (v[j].x + v[j].y) + (v[j].z + v[j].w); }
;     ...
; #pragma unroll
;         for (int j = 0; j < 8; ++j) { const int c = 4 * lane + 256 * j; const f32x4 gg = *(const f32x4*)(g1 + c), bb = *(const f32x4*)(b1 + c);
;             const f32x4 o = v[j] * rstd * gg + bb;
;             u32x2 wh; wh.x = pk2(o.x, o.y); wh.y = pk2(o.z, o.w); *(u32x2*)(x1b + (size_t)t * D + c) = wh;
;             u32x2 wl; wl.x = pk2(o.x - bflo(wh.x), o.y - bfhi(wh.x)); wl.y = pk2(o.z - bflo(wh.y), o.w - bfhi(wh.y)); *(u32x2*)(x1l + (size_t)t * D + c) = wl;
;             if (x1q) *(unsigned*)(x1q + (size_t)t * D + c) = pk4_fp8(o.x, o.y, o.z, o.w); }
	global_store_dwordx2 v[80:81], v[102:103], off offset:512
	global_store_dword v[70:71], v17, off offset:256
	v_mov_b64_e32 v[98:99], v[136:137]
	v_mov_b64_e32 v[100:101], v[138:139]
	s_nop 0
	v_mov_b64_e32 v[102:103], v[168:169]
	v_mov_b64_e32 v[104:105], v[170:171]
	v_mov_b32_e32 v17, v193
	v_pk_fma_f32 v[94:95], v[94:95], v[98:99], v[102:103]
	s_nop 0
	v_cvt_pk_fp8_f32 v17, v94, v95
	v_cvt_pk_bf16_f32 v98, v94, v95
	v_pk_fma_f32 v[96:97], v[96:97], v[100:101], v[104:105]
	v_lshlrev_b32_e32 v100, 16, v98
	v_and_b32_e32 v101, 0xffff0000, v98
	v_cvt_pk_bf16_f32 v99, v96, v97
	v_pk_add_f32 v[100:101], v[94:95], v[100:101] neg_lo:[0,1] neg_hi:[0,1]
	v_cvt_pk_fp8_f32 v17, v96, v97 op_sel:[0,0,1]
	global_store_dwordx2 v[78:79], v[98:99], off offset:1024
	v_cvt_pk_bf16_f32 v98, v100, v101
	v_lshlrev_b32_e32 v100, 16, v99
	v_and_b32_e32 v101, 0xffff0000, v99
	v_pk_add_f32 v[100:101], v[96:97], v[100:101] neg_lo:[0,1] neg_hi:[0,1]
	s_nop 0
	v_cvt_pk_bf16_f32 v99, v100, v101
	global_store_dwordx2 v[80:81], v[98:99], off offset:1024
	global_store_dword v[70:71], v17, off offset:512
	v_mov_b64_e32 v[94:95], v[140:141]
	v_mov_b64_e32 v[96:97], v[142:143]
	s_nop 0
	v_mov_b64_e32 v[98:99], v[172:173]
	v_mov_b64_e32 v[100:101], v[174:175]
	v_mov_b32_e32 v17, v193
	v_pk_fma_f32 v[90:91], v[90:91], v[94:95], v[98:99]
	s_nop 0
	v_cvt_pk_fp8_f32 v17, v90, v91
	v_cvt_pk_bf16_f32 v94, v90, v91
	v_pk_fma_f32 v[92:93], v[92:93], v[96:97], v[100:101]
	v_lshlrev_b32_e32 v96, 16, v94
	v_and_b32_e32 v97, 0xffff0000, v94
	v_cvt_pk_bf16_f32 v95, v92, v93
	v_pk_add_f32 v[96:97], v[90:91], v[96:97] neg_lo:[0,1] neg_hi:[0,1]
	v_cvt_pk_fp8_f32 v17, v92, v93 op_sel:[0,0,1]
	global_store_dwordx2 v[78:79], v[94:95], off offset:1536
	v_cvt_pk_bf16_f32 v94, v96, v97
	v_lshlrev_b32_e32 v96, 16, v95
	v_and_b32_e32 v97, 0xffff0000, v95
	v_pk_add_f32 v[96:97], v[92:93], v[96:97] neg_lo:[0,1] neg_hi:[0,1]
	s_nop 0
	v_cvt_pk_bf16_f32 v95, v96, v97
	global_store_dwordx2 v[80:81], v[94:95], off offset:1536
	global_store_dword v[70:71], v17, off offset:768
	v_mov_b64_e32 v[90:91], v[144:145]
	v_mov_b64_e32 v[92:93], v[146:147]
	s_nop 0
	v_mov_b64_e32 v[94:95], v[176:177]
	v_mov_b64_e32 v[96:97], v[178:179]
	v_mov_b32_e32 v17, v193
	v_pk_fma_f32 v[86:87], v[86:87], v[90:91], v[94:95]
	s_nop 0
	v_cvt_pk_fp8_f32 v17, v86, v87
	v_cvt_pk_bf16_f32 v90, v86, v87
	v_pk_fma_f32 v[88:89], v[88:89], v[92:93], v[96:97]
	v_lshlrev_b32_e32 v92, 16, v90
	v_and_b32_e32 v93, 0xffff0000, v90
	v_cvt_pk_bf16_f32 v91, v88, v89
	v_pk_add_f32 v[92:93], v[86:87], v[92:93] neg_lo:[0,1] neg_hi:[0,1]
	v_cvt_pk_fp8_f32 v17, v88, v89 op_sel:[0,0,1]
	global_store_dwordx2 v[78:79], v[90:91], off offset:2048
	v_cvt_pk_bf16_f32 v90, v92, v93
	v_lshlrev_b32_e32 v92, 16, v91
	v_and_b32_e32 v93, 0xffff0000, v91
	v_pk_add_f32 v[92:93], v[88:89], v[92:93] neg_lo:[0,1] neg_hi:[0,1]
	s_nop 0
	v_cvt_pk_bf16_f32 v91, v92, v93
	global_store_dwordx2 v[80:81], v[90:91], off offset:2048
	global_store_dword v[70:71], v17, off offset:1024
	v_mov_b64_e32 v[86:87], v[148:149]
	v_mov_b64_e32 v[88:89], v[150:151]
	s_nop 0
	v_mov_b64_e32 v[90:91], v[180:181]
	v_mov_b64_e32 v[92:93], v[182:183]
	v_mov_b32_e32 v17, v193
	v_pk_fma_f32 v[82:83], v[82:83], v[86:87], v[90:91]
	s_nop 0
	v_cvt_pk_fp8_f32 v17, v82, v83
	v_cvt_pk_bf16_f32 v86, v82, v83
	v_pk_fma_f32 v[84:85], v[84:85], v[88:89], v[92:93]
	v_lshlrev_b32_e32 v88, 16, v86
	v_and_b32_e32 v89, 0xffff0000, v86
	v_cvt_pk_bf16_f32 v87, v84, v85
	v_pk_add_f32 v[88:89], v[82:83], v[88:89] neg_lo:[0,1] neg_hi:[0,1]
	v_cvt_pk_fp8_f32 v17, v84, v85 op_sel:[0,0,1]
	global_store_dwordx2 v[78:79], v[86:87], off offset:2560
	v_cvt_pk_bf16_f32 v86, v88, v89
	v_lshlrev_b32_e32 v88, 16, v87
	v_and_b32_e32 v89, 0xffff0000, v87
	v_pk_add_f32 v[88:89], v[84:85], v[88:89] neg_lo:[0,1] neg_hi:[0,1]
	v_lshlrev_b32_e32 v92, 16, v65
	v_cvt_pk_bf16_f32 v87, v88, v89
	global_store_dwordx2 v[80:81], v[86:87], off offset:2560
	global_store_dword v[70:71], v17, off offset:1280
	v_mov_b64_e32 v[82:83], v[152:153]
	v_mov_b64_e32 v[84:85], v[154:155]
	s_nop 0
	v_mov_b64_e32 v[86:87], v[184:185]
	v_mov_b64_e32 v[88:89], v[186:187]
	v_mov_b32_e32 v17, v193
	v_and_b32_e32 v93, 0xffff0000, v65
	v_add_f32_e32 v19, v92, v93
	v_pk_fma_f32 v[74:75], v[74:75], v[82:83], v[86:87]
	s_nop 0
	v_cvt_pk_fp8_f32 v17, v74, v75
	v_cvt_pk_bf16_f32 v82, v74, v75
	v_pk_fma_f32 v[76:77], v[76:77], v[84:85], v[88:89]
	v_lshlrev_b32_e32 v84, 16, v82
	v_and_b32_e32 v85, 0xffff0000, v82
	v_cvt_pk_bf16_f32 v83, v76, v77
	v_pk_add_f32 v[84:85], v[74:75], v[84:85] neg_lo:[0,1] neg_hi:[0,1]
	v_cvt_pk_fp8_f32 v17, v76, v77 op_sel:[0,0,1]
	global_store_dwordx2 v[78:79], v[82:83], off offset:3072
	v_cvt_pk_bf16_f32 v82, v84, v85
	v_lshlrev_b32_e32 v84, 16, v83
	v_and_b32_e32 v85, 0xffff0000, v83
	v_pk_add_f32 v[84:85], v[76:77], v[84:85] neg_lo:[0,1] neg_hi:[0,1]
	v_lshlrev_b32_e32 v86, 16, v64
	v_cvt_pk_bf16_f32 v83, v84, v85
	global_store_dwordx2 v[80:81], v[82:83], off offset:3072
	global_store_dword v[70:71], v17, off offset:1536
	v_mov_b64_e32 v[74:75], v[156:157]
	v_mov_b64_e32 v[76:77], v[158:159]
	s_nop 0
	v_mov_b64_e32 v[82:83], v[188:189]
	v_mov_b64_e32 v[84:85], v[190:191]
	v_mov_b32_e32 v17, v193
	v_and_b32_e32 v87, 0xffff0000, v64
	v_pk_fma_f32 v[68:69], v[68:69], v[74:75], v[82:83]
	s_nop 0
	v_cvt_pk_fp8_f32 v17, v68, v69
	v_cvt_pk_bf16_f32 v72, v68, v69
	v_pk_fma_f32 v[66:67], v[66:67], v[76:77], v[84:85]
	v_lshlrev_b32_e32 v74, 16, v72
	v_and_b32_e32 v75, 0xffff0000, v72
	v_cvt_pk_bf16_f32 v73, v66, v67
	v_pk_add_f32 v[74:75], v[68:69], v[74:75] neg_lo:[0,1] neg_hi:[0,1]
	v_cvt_pk_fp8_f32 v17, v66, v67 op_sel:[0,0,1]
; __device__ __forceinline__ void ln_router_tile(const Frame& F, const bf16* yf, const float* g1, const float* b1, bf16* x1b, bf16* x1l, unsigned char* x1q, const bf16* __restrict__ rthi, const bf16* __restrict__ rtlo, ...
;     ...
;         for (int j = 0; j < 8; ++j) { const u32x2 y = yraw[r4][j]; v[j] = (f32x4){bflo(y.x), bfhi(y.x), bflo(y.y), bfhi(y.y)}; s += (v[j].x + v[j].y) + (v[j].z + v[j].w); }
;         const float mean = wave_sum(s) * (1.0f / D); float s2 = 0.f;
; #pragma unroll
;         for (int j = 0; j < 8; ++j) { v[j] = v[j] - mean; s2 += (v[j].x * v[j].x + v[j].y * v[j].y) + (v[j].z * v[j].z + v[j].w * v[j].w); }
;         const float rstd = rsqrtf(wave_sum(s2) * (1.0f / D) + EPS);
	global_store_dwordx2 v[78:79], v[72:73], off offset:3584
	v_cvt_pk_bf16_f32 v72, v74, v75
	v_lshlrev_b32_e32 v74, 16, v73
	v_and_b32_e32 v75, 0xffff0000, v73
	v_pk_add_f32 v[74:75], v[66:67], v[74:75] neg_lo:[0,1] neg_hi:[0,1]
	v_lshlrev_b32_e32 v82, 16, v62
	v_cvt_pk_bf16_f32 v73, v74, v75
	global_store_dwordx2 v[80:81], v[72:73], off offset:3584
	global_store_dword v[70:71], v17, off offset:1792
	v_add_f32_e32 v17, v86, v87
	v_and_b32_e32 v83, 0xffff0000, v62
	v_lshlrev_b32_e32 v84, 16, v63
	v_and_b32_e32 v85, 0xffff0000, v63
	v_add_f32_e32 v17, v17, v19
	v_add_f32_e32 v19, v82, v83
	v_add_f32_e32 v21, v84, v85
	v_add_f32_e32 v17, 0, v17
	v_add_f32_e32 v19, v19, v21
	v_lshlrev_b32_e32 v78, 16, v60
	v_and_b32_e32 v79, 0xffff0000, v60
	v_lshlrev_b32_e32 v80, 16, v61
	v_and_b32_e32 v81, 0xffff0000, v61
	v_add_f32_e32 v17, v17, v19
	v_add_f32_e32 v19, v78, v79
	v_add_f32_e32 v21, v80, v81
	v_add_f32_e32 v19, v19, v21
	v_lshlrev_b32_e32 v74, 16, v58
	v_and_b32_e32 v75, 0xffff0000, v58
	v_lshlrev_b32_e32 v76, 16, v59
	v_and_b32_e32 v77, 0xffff0000, v59
	v_add_f32_e32 v17, v17, v19
	v_add_f32_e32 v19, v74, v75
	v_add_f32_e32 v21, v76, v77
	v_add_f32_e32 v19, v19, v21
	v_lshlrev_b32_e32 v70, 16, v56
	v_and_b32_e32 v71, 0xffff0000, v56
	v_lshlrev_b32_e32 v72, 16, v57
	v_and_b32_e32 v73, 0xffff0000, v57
	v_add_f32_e32 v17, v17, v19
	v_add_f32_e32 v19, v70, v71
	v_add_f32_e32 v21, v72, v73
	v_add_f32_e32 v19, v19, v21
	v_lshlrev_b32_e32 v66, 16, v54
	v_and_b32_e32 v67, 0xffff0000, v54
	v_lshlrev_b32_e32 v68, 16, v55
	v_and_b32_e32 v69, 0xffff0000, v55
	v_add_f32_e32 v17, v17, v19
	v_add_f32_e32 v19, v66, v67
	v_add_f32_e32 v21, v68, v69
	v_add_f32_e32 v19, v19, v21
	v_lshlrev_b32_e32 v58, 16, v52
	v_and_b32_e32 v59, 0xffff0000, v52
	v_lshlrev_b32_e32 v60, 16, v53
	v_and_b32_e32 v61, 0xffff0000, v53
	v_add_f32_e32 v17, v17, v19
	v_add_f32_e32 v19, v58, v59
	v_add_f32_e32 v21, v60, v61
	v_add_f32_e32 v19, v19, v21
	v_lshlrev_b32_e32 v52, 16, v50
	v_and_b32_e32 v53, 0xffff0000, v50
	v_lshlrev_b32_e32 v50, 16, v51
	v_and_b32_e32 v51, 0xffff0000, v51
	v_add_f32_e32 v17, v17, v19
	v_add_f32_e32 v19, v52, v53
	v_add_f32_e32 v21, v50, v51
	v_add_f32_e32 v19, v19, v21
	v_add_f32_e32 v17, v17, v19
	s_nop 1
	v_add_f32_dpp v17, v17, v17 quad_perm:[1,0,3,2] row_mask:0xf bank_mask:0xf bound_ctrl:1
	s_nop 1
	v_add_f32_dpp v17, v17, v17 quad_perm:[2,3,0,1] row_mask:0xf bank_mask:0xf bound_ctrl:1
	s_nop 1
	v_add_f32_dpp v17, v17, v17 row_half_mirror row_mask:0xf bank_mask:0xf bound_ctrl:1
	s_nop 1
	v_add_f32_dpp v17, v17, v17 row_mirror row_mask:0xf bank_mask:0xf bound_ctrl:1
	v_mov_b32_e32 v19, v17
	s_nop 1
	v_permlane32_swap_b32 v17, v19
	s_nop 0
	v_add_f32_e32 v17, v17, v19
	s_nop 0
	v_readlane_b32 s9, v17, 16
	v_readlane_b32 s8, v17, 0
	s_nop 0
	v_mov_b32_e32 v17, s9
	v_add_f32_e32 v17, s8, v17
	v_fmac_f32_e32 v93, 0xba000000, v17
	v_fmac_f32_e32 v87, 0xba000000, v17
	v_fmac_f32_e32 v92, 0xba000000, v17
	v_fmac_f32_e32 v86, 0xba000000, v17
	v_mul_f32_e32 v19, v87, v87
	v_mul_f32_e32 v21, v93, v93
	v_fmac_f32_e32 v19, v86, v86
	v_fmac_f32_e32 v21, v92, v92
	v_fmac_f32_e32 v85, 0xba000000, v17
	v_fmac_f32_e32 v83, 0xba000000, v17
	v_add_f32_e32 v19, v19, v21
	v_fmac_f32_e32 v84, 0xba000000, v17
	v_fmac_f32_e32 v82, 0xba000000, v17
	v_mul_f32_e32 v21, v83, v83
	v_mul_f32_e32 v54, v85, v85
	v_fmac_f32_e32 v21, v82, v82
	v_fmac_f32_e32 v54, v84, v84
	v_add_f32_e32 v21, v21, v54
	v_fmac_f32_e32 v81, 0xba000000, v17
	v_fmac_f32_e32 v79, 0xba000000, v17
	v_add_f32_e32 v19, v19, v21
	v_fmac_f32_e32 v80, 0xba000000, v17
	v_fmac_f32_e32 v78, 0xba000000, v17
	v_mul_f32_e32 v21, v79, v79
	v_mul_f32_e32 v54, v81, v81
	v_fmac_f32_e32 v21, v78, v78
	v_fmac_f32_e32 v54, v80, v80
	v_add_f32_e32 v21, v21, v54
	v_fmac_f32_e32 v77, 0xba000000, v17
	v_fmac_f32_e32 v75, 0xba000000, v17
	v_add_f32_e32 v19, v21, v19
	v_fmac_f32_e32 v76, 0xba000000, v17
	v_fmac_f32_e32 v74, 0xba000000, v17
	v_mul_f32_e32 v21, v75, v75
	v_mul_f32_e32 v54, v77, v77
	v_fmac_f32_e32 v21, v74, v74
	v_fmac_f32_e32 v54, v76, v76
	v_add_f32_e32 v21, v21, v54
	v_fmac_f32_e32 v73, 0xba000000, v17
	v_fmac_f32_e32 v71, 0xba000000, v17
	v_add_f32_e32 v19, v21, v19
	v_fmac_f32_e32 v72, 0xba000000, v17
	v_fmac_f32_e32 v70, 0xba000000, v17
	v_mul_f32_e32 v21, v71, v71
	v_mul_f32_e32 v54, v73, v73
	v_fmac_f32_e32 v21, v70, v70
	v_fmac_f32_e32 v54, v72, v72
	v_add_f32_e32 v21, v21, v54
	v_fmac_f32_e32 v69, 0xba000000, v17
	v_fmac_f32_e32 v67, 0xba000000, v17
	v_add_f32_e32 v19, v21, v19
	v_fmac_f32_e32 v68, 0xba000000, v17
	v_fmac_f32_e32 v66, 0xba000000, v17
	v_mul_f32_e32 v21, v67, v67
	v_mul_f32_e32 v54, v69, v69
	v_fmac_f32_e32 v21, v66, v66
	v_fmac_f32_e32 v54, v68, v68
	v_add_f32_e32 v21, v21, v54
	v_fmac_f32_e32 v61, 0xba000000, v17
	v_fmac_f32_e32 v59, 0xba000000, v17
	v_add_f32_e32 v19, v21, v19
	v_fmac_f32_e32 v60, 0xba000000, v17
	v_fmac_f32_e32 v58, 0xba000000, v17
	v_mul_f32_e32 v21, v59, v59
	v_mul_f32_e32 v54, v61, v61
	v_fmac_f32_e32 v21, v58, v58
	v_fmac_f32_e32 v54, v60, v60
	v_add_f32_e32 v21, v21, v54
	v_fmac_f32_e32 v51, 0xba000000, v17
	v_fmac_f32_e32 v53, 0xba000000, v17
	v_add_f32_e32 v19, v21, v19
	v_fmac_f32_e32 v50, 0xba000000, v17
	v_fmac_f32_e32 v52, 0xba000000, v17
	v_mul_f32_e32 v17, v53, v53
	v_mul_f32_e32 v21, v51, v51
	v_fmac_f32_e32 v17, v52, v52
	v_fmac_f32_e32 v21, v50, v50
	v_add_f32_e32 v17, v17, v21
	v_add_f32_e32 v17, v17, v19
	s_nop 1
	v_add_f32_dpp v17, v17, v17 quad_perm:[1,0,3,2] row_mask:0xf bank_mask:0xf bound_ctrl:1
	s_nop 1
	v_add_f32_dpp v17, v17, v17 quad_perm:[2,3,0,1] row_mask:0xf bank_mask:0xf bound_ctrl:1
	s_nop 1
	v_add_f32_dpp v17, v17, v17 row_half_mirror row_mask:0xf bank_mask:0xf bound_ctrl:1
; __device__ __forceinline__ unsigned pk2(float lo, float hi) { return hw_pk_bf16(lo, hi); }
; __device__ __forceinline__ unsigned pk4_fp8(float a, float b, float c, float d) { int w = __builtin_amdgcn_cvt_pk_fp8_f32(a, b, 0, false); w = __builtin_amdgcn_cvt_pk_fp8_f32(c, d, w, true); return (unsigned)w; }
; __device__ __forceinline__ void ln_router_tile(const Frame& F, const bf16* yf, const float* g1, const float* b1, bf16* x1b, bf16* x1l, unsigned char* x1q, const bf16* __restrict__ rthi, const bf16* __restrict__ rtlo, ...
;     ...
;         const float rstd = rsqrtf(wave_sum(s2) * (1.0f / D) + EPS);
; #pragma unroll
;         for (int j = 0; j < 8; ++j) { const int c = 4 * lane + 256 * j; const f32x4 gg = *(const f32x4*)(g1 + c), bb = *(const f32x4*)(b1 + c);
;             const f32x4 o = v[j] * rstd * gg + bb;
;             u32x2 wh; wh.x = pk2(o.x, o.y); wh.y = pk2(o.z, o.w); *(u32x2*)(x1b + (size_t)t * D + c) = wh;
;             u32x2 wl; wl.x = pk2(o.x - bflo(wh.x), o.y - bfhi(wh.x)); wl.y = pk2(o.z - bflo(wh.y), o.w - bfhi(wh.y)); *(u32x2*)(x1l + (size_t)t * D + c) = wl;
;             if (x1q) *(unsigned*)(x1q + (size_t)t * D + c) = pk4_fp8(o.x, o.y, o.z, o.w); }
	s_nop 1
	v_add_f32_dpp v17, v17, v17 row_mirror row_mask:0xf bank_mask:0xf bound_ctrl:1
	v_mov_b32_e32 v19, v17
	s_nop 1
	v_permlane32_swap_b32 v17, v19
	v_mov_b64_e32 v[62:63], v[128:129]
	v_mov_b64_e32 v[64:65], v[130:131]
	v_mov_b64_e32 v[88:89], v[160:161]
	v_mov_b64_e32 v[90:91], v[162:163]
	v_add_f32_e32 v17, v17, v19
	s_nop 0
	v_readlane_b32 s9, v17, 16
	v_readlane_b32 s8, v17, 0
	s_nop 0
	v_mov_b32_e32 v17, s9
	v_add_f32_e32 v17, s8, v17
	v_fmamk_f32 v17, v17, 0x3a000000, v194
	v_cmp_gt_f32_e64 s[36:37], s26, v17
	v_mul_f32_e32 v19, 0x4b800000, v17
	s_nop 0
	v_cndmask_b32_e64 v17, v17, v19, s[36:37]
	v_rsq_f32_e32 v17, v17
	s_nop 0
	v_mul_f32_e32 v19, 0x45800000, v17
	v_cndmask_b32_e64 v56, v17, v19, s[36:37]
	v_pk_mul_f32 v[54:55], v[86:87], v[56:57] op_sel_hi:[1,0]
	v_mov_b32_e32 v17, v193
	v_pk_mul_f32 v[86:87], v[92:93], v[56:57] op_sel_hi:[1,0]
	v_pk_mul_f32 v[82:83], v[82:83], v[56:57] op_sel_hi:[1,0]
	v_pk_mul_f32 v[84:85], v[84:85], v[56:57] op_sel_hi:[1,0]
	v_pk_mul_f32 v[78:79], v[78:79], v[56:57] op_sel_hi:[1,0]
	v_pk_mul_f32 v[80:81], v[80:81], v[56:57] op_sel_hi:[1,0]
	v_pk_mul_f32 v[74:75], v[74:75], v[56:57] op_sel_hi:[1,0]
	v_pk_mul_f32 v[76:77], v[76:77], v[56:57] op_sel_hi:[1,0]
	v_pk_mul_f32 v[70:71], v[70:71], v[56:57] op_sel_hi:[1,0]
	v_pk_mul_f32 v[72:73], v[72:73], v[56:57] op_sel_hi:[1,0]
	v_pk_mul_f32 v[66:67], v[66:67], v[56:57] op_sel_hi:[1,0]
	v_pk_mul_f32 v[68:69], v[68:69], v[56:57] op_sel_hi:[1,0]
	v_pk_mul_f32 v[58:59], v[58:59], v[56:57] op_sel_hi:[1,0]
	v_pk_mul_f32 v[60:61], v[60:61], v[56:57] op_sel_hi:[1,0]
	v_pk_mul_f32 v[52:53], v[52:53], v[56:57] op_sel_hi:[1,0]
	v_pk_mul_f32 v[50:51], v[50:51], v[56:57] op_sel_hi:[1,0]
	v_pk_fma_f32 v[88:89], v[62:63], v[54:55], v[88:89]
	s_nop 0
	v_cvt_pk_fp8_f32 v17, v88, v89
	v_cvt_pk_bf16_f32 v54, v88, v89
	v_pk_fma_f32 v[86:87], v[64:65], v[86:87], v[90:91]
	v_lshlrev_b32_e32 v64, 16, v54
	v_and_b32_e32 v65, 0xffff0000, v54
	v_cvt_pk_bf16_f32 v55, v86, v87
	v_lshl_add_u64 v[62:63], v[28:29], 0, s[4:5]
	v_pk_add_f32 v[64:65], v[88:89], v[64:65] neg_lo:[0,1] neg_hi:[0,1]
	global_store_dwordx2 v[62:63], v[54:55], off
	v_cvt_pk_bf16_f32 v54, v64, v65
	v_lshlrev_b32_e32 v64, 16, v55
	v_and_b32_e32 v65, 0xffff0000, v55
	v_cvt_pk_fp8_f32 v17, v86, v87 op_sel:[0,0,1]
	v_pk_add_f32 v[64:65], v[86:87], v[64:65] neg_lo:[0,1] neg_hi:[0,1]
	s_nop 0
	v_cvt_pk_bf16_f32 v55, v64, v65
	v_lshl_add_u64 v[64:65], v[30:31], 0, s[4:5]
	global_store_dwordx2 v[64:65], v[54:55], off
	v_lshl_add_u64 v[54:55], v[32:33], 0, s[6:7]
	global_store_dword v[54:55], v17, off
	v_mov_b64_e32 v[86:87], v[132:133]
	v_mov_b64_e32 v[88:89], v[134:135]
	v_mov_b64_e32 v[90:91], v[164:165]
	v_mov_b64_e32 v[92:93], v[166:167]
	v_mov_b32_e32 v17, v193
	s_mov_b32 s6, 4
	v_pk_fma_f32 v[82:83], v[86:87], v[82:83], v[90:91]
	s_nop 0
	v_cvt_pk_fp8_f32 v17, v82, v83
	v_cvt_pk_bf16_f32 v86, v82, v83
	v_pk_fma_f32 v[84:85], v[88:89], v[84:85], v[92:93]
	v_lshlrev_b32_e32 v88, 16, v86
	v_and_b32_e32 v89, 0xffff0000, v86
	v_cvt_pk_bf16_f32 v87, v84, v85
	v_pk_add_f32 v[88:89], v[82:83], v[88:89] neg_lo:[0,1] neg_hi:[0,1]
	v_cvt_pk_fp8_f32 v17, v84, v85 op_sel:[0,0,1]
	global_store_dwordx2 v[62:63], v[86:87], off offset:512
	v_cvt_pk_bf16_f32 v86, v88, v89
	v_lshlrev_b32_e32 v88, 16, v87
	v_and_b32_e32 v89, 0xffff0000, v87
	v_pk_add_f32 v[88:89], v[84:85], v[88:89] neg_lo:[0,1] neg_hi:[0,1]
	s_nop 0
	v_cvt_pk_bf16_f32 v87, v88, v89
	global_store_dwordx2 v[64:65], v[86:87], off offset:512
	global_store_dword v[54:55], v17, off offset:256
	v_mov_b64_e32 v[82:83], v[136:137]
	v_mov_b64_e32 v[84:85], v[138:139]
	s_nop 0
	v_mov_b64_e32 v[86:87], v[168:169]
	v_mov_b64_e32 v[88:89], v[170:171]
	v_mov_b32_e32 v17, v193
	v_pk_fma_f32 v[78:79], v[78:79], v[82:83], v[86:87]
	s_nop 0
	v_cvt_pk_fp8_f32 v17, v78, v79
	v_cvt_pk_bf16_f32 v82, v78, v79
	v_pk_fma_f32 v[80:81], v[80:81], v[84:85], v[88:89]
	v_lshlrev_b32_e32 v84, 16, v82
	v_and_b32_e32 v85, 0xffff0000, v82
	v_cvt_pk_bf16_f32 v83, v80, v81
	v_pk_add_f32 v[84:85], v[78:79], v[84:85] neg_lo:[0,1] neg_hi:[0,1]
	v_cvt_pk_fp8_f32 v17, v80, v81 op_sel:[0,0,1]
	global_store_dwordx2 v[62:63], v[82:83], off offset:1024
	v_cvt_pk_bf16_f32 v82, v84, v85
	v_lshlrev_b32_e32 v84, 16, v83
	v_and_b32_e32 v85, 0xffff0000, v83
	v_pk_add_f32 v[84:85], v[80:81], v[84:85] neg_lo:[0,1] neg_hi:[0,1]
	s_nop 0
	v_cvt_pk_bf16_f32 v83, v84, v85
	global_store_dwordx2 v[64:65], v[82:83], off offset:1024
	global_store_dword v[54:55], v17, off offset:512
	v_mov_b64_e32 v[78:79], v[140:141]
	v_mov_b64_e32 v[80:81], v[142:143]
	s_nop 0
	v_mov_b64_e32 v[82:83], v[172:173]
	v_mov_b64_e32 v[84:85], v[174:175]
	v_mov_b32_e32 v17, v193
	v_pk_fma_f32 v[74:75], v[74:75], v[78:79], v[82:83]
	s_nop 0
	v_cvt_pk_fp8_f32 v17, v74, v75
	v_cvt_pk_bf16_f32 v78, v74, v75
	v_pk_fma_f32 v[76:77], v[76:77], v[80:81], v[84:85]
	v_lshlrev_b32_e32 v80, 16, v78
	v_and_b32_e32 v81, 0xffff0000, v78
	v_cvt_pk_bf16_f32 v79, v76, v77
	v_pk_add_f32 v[80:81], v[74:75], v[80:81] neg_lo:[0,1] neg_hi:[0,1]
	v_cvt_pk_fp8_f32 v17, v76, v77 op_sel:[0,0,1]
	global_store_dwordx2 v[62:63], v[78:79], off offset:1536
	v_cvt_pk_bf16_f32 v78, v80, v81
	v_lshlrev_b32_e32 v80, 16, v79
	v_and_b32_e32 v81, 0xffff0000, v79
	v_pk_add_f32 v[80:81], v[76:77], v[80:81] neg_lo:[0,1] neg_hi:[0,1]
	s_nop 0
	v_cvt_pk_bf16_f32 v79, v80, v81
	global_store_dwordx2 v[64:65], v[78:79], off offset:1536
	global_store_dword v[54:55], v17, off offset:768
	v_mov_b64_e32 v[74:75], v[144:145]
	v_mov_b64_e32 v[76:77], v[146:147]
	s_nop 0
	v_mov_b64_e32 v[78:79], v[176:177]
	v_mov_b64_e32 v[80:81], v[178:179]
	v_mov_b32_e32 v17, v193
; __device__ __forceinline__ unsigned pk2(float lo, float hi) { return hw_pk_bf16(lo, hi); }
; __device__ __forceinline__ unsigned pk4_fp8(float a, float b, float c, float d) { int w = __builtin_amdgcn_cvt_pk_fp8_f32(a, b, 0, false); w = __builtin_amdgcn_cvt_pk_fp8_f32(c, d, w, true); return (unsigned)w; }
; __device__ __forceinline__ void ln_router_tile(const Frame& F, const bf16* yf, const float* g1, const float* b1, bf16* x1b, bf16* x1l, unsigned char* x1q, const bf16* __restrict__ rthi, const bf16* __restrict__ rtlo, ...
;     ...
;         for (int j = 0; j < 8; ++j) { const u32x2 y = yraw[r4][j]; v[j] = (f32x4){bflo(y.x), bfhi(y.x), bflo(y.y), bfhi(y.y)}; s += (v[j].x + v[j].y) + (v[j].z + v[j].w); }
;     ...
; #pragma unroll
;         for (int j = 0; j < 8; ++j) { const int c = 4 * lane + 256 * j; const f32x4 gg = *(const f32x4*)(g1 + c), bb = *(const f32x4*)(b1 + c);
;             const f32x4 o = v[j] * rstd * gg + bb;
;             u32x2 wh; wh.x = pk2(o.x, o.y); wh.y = pk2(o.z, o.w); *(u32x2*)(x1b + (size_t)t * D + c) = wh;
;             u32x2 wl; wl.x = pk2(o.x - bflo(wh.x), o.y - bfhi(wh.x)); wl.y = pk2(o.z - bflo(wh.y), o.w - bfhi(wh.y)); *(u32x2*)(x1l + (size_t)t * D + c) = wl;
;             if (x1q) *(unsigned*)(x1q + (size_t)t * D + c) = pk4_fp8(o.x, o.y, o.z, o.w); }
	v_pk_fma_f32 v[70:71], v[70:71], v[74:75], v[78:79]
	s_nop 0
	v_cvt_pk_fp8_f32 v17, v70, v71
	v_cvt_pk_bf16_f32 v74, v70, v71
	v_pk_fma_f32 v[72:73], v[72:73], v[76:77], v[80:81]
	v_lshlrev_b32_e32 v76, 16, v74
	v_and_b32_e32 v77, 0xffff0000, v74
	v_cvt_pk_bf16_f32 v75, v72, v73
	v_pk_add_f32 v[76:77], v[70:71], v[76:77] neg_lo:[0,1] neg_hi:[0,1]
	v_cvt_pk_fp8_f32 v17, v72, v73 op_sel:[0,0,1]
	global_store_dwordx2 v[62:63], v[74:75], off offset:2048
	v_cvt_pk_bf16_f32 v74, v76, v77
	v_lshlrev_b32_e32 v76, 16, v75
	v_and_b32_e32 v77, 0xffff0000, v75
	v_pk_add_f32 v[76:77], v[72:73], v[76:77] neg_lo:[0,1] neg_hi:[0,1]
	s_nop 0
	v_cvt_pk_bf16_f32 v75, v76, v77
	global_store_dwordx2 v[64:65], v[74:75], off offset:2048
	global_store_dword v[54:55], v17, off offset:1024
	v_mov_b64_e32 v[70:71], v[148:149]
	v_mov_b64_e32 v[72:73], v[150:151]
	s_nop 0
	v_mov_b64_e32 v[74:75], v[180:181]
	v_mov_b64_e32 v[76:77], v[182:183]
	v_mov_b32_e32 v17, v193
	v_pk_fma_f32 v[66:67], v[66:67], v[70:71], v[74:75]
	s_nop 0
	v_cvt_pk_fp8_f32 v17, v66, v67
	v_cvt_pk_bf16_f32 v70, v66, v67
	v_pk_fma_f32 v[68:69], v[68:69], v[72:73], v[76:77]
	v_lshlrev_b32_e32 v72, 16, v70
	v_and_b32_e32 v73, 0xffff0000, v70
	v_cvt_pk_bf16_f32 v71, v68, v69
	v_pk_add_f32 v[72:73], v[66:67], v[72:73] neg_lo:[0,1] neg_hi:[0,1]
	v_cvt_pk_fp8_f32 v17, v68, v69 op_sel:[0,0,1]
	global_store_dwordx2 v[62:63], v[70:71], off offset:2560
	v_cvt_pk_bf16_f32 v70, v72, v73
	v_lshlrev_b32_e32 v72, 16, v71
	v_and_b32_e32 v73, 0xffff0000, v71
	v_pk_add_f32 v[72:73], v[68:69], v[72:73] neg_lo:[0,1] neg_hi:[0,1]
	v_lshlrev_b32_e32 v76, 16, v49
	v_cvt_pk_bf16_f32 v71, v72, v73
	global_store_dwordx2 v[64:65], v[70:71], off offset:2560
	global_store_dword v[54:55], v17, off offset:1280
	v_mov_b64_e32 v[66:67], v[152:153]
	v_mov_b64_e32 v[68:69], v[154:155]
	s_nop 0
	v_mov_b64_e32 v[70:71], v[184:185]
	v_mov_b64_e32 v[72:73], v[186:187]
	v_mov_b32_e32 v17, v193
	v_and_b32_e32 v77, 0xffff0000, v49
	v_add_f32_e32 v19, v76, v77
	v_and_b32_e32 v49, 0xffff0000, v35
	v_pk_fma_f32 v[58:59], v[58:59], v[66:67], v[70:71]
	s_nop 0
	v_cvt_pk_fp8_f32 v17, v58, v59
	v_cvt_pk_bf16_f32 v66, v58, v59
	v_pk_fma_f32 v[60:61], v[60:61], v[68:69], v[72:73]
	v_lshlrev_b32_e32 v68, 16, v66
	v_and_b32_e32 v69, 0xffff0000, v66
	v_cvt_pk_bf16_f32 v67, v60, v61
	v_pk_add_f32 v[68:69], v[58:59], v[68:69] neg_lo:[0,1] neg_hi:[0,1]
	v_cvt_pk_fp8_f32 v17, v60, v61 op_sel:[0,0,1]
	global_store_dwordx2 v[62:63], v[66:67], off offset:3072
	v_cvt_pk_bf16_f32 v66, v68, v69
	v_lshlrev_b32_e32 v68, 16, v67
	v_and_b32_e32 v69, 0xffff0000, v67
	v_pk_add_f32 v[68:69], v[60:61], v[68:69] neg_lo:[0,1] neg_hi:[0,1]
	v_lshlrev_b32_e32 v70, 16, v48
	v_cvt_pk_bf16_f32 v67, v68, v69
	global_store_dwordx2 v[64:65], v[66:67], off offset:3072
	global_store_dword v[54:55], v17, off offset:1536
	v_mov_b64_e32 v[58:59], v[156:157]
	v_mov_b64_e32 v[60:61], v[158:159]
	s_nop 0
	v_mov_b64_e32 v[66:67], v[188:189]
	v_mov_b64_e32 v[68:69], v[190:191]
	v_mov_b32_e32 v17, v193
	v_and_b32_e32 v71, 0xffff0000, v48
	v_lshlrev_b32_e32 v48, 16, v35
	v_and_b32_e32 v35, 0xffff0000, v36
	v_pk_fma_f32 v[52:53], v[52:53], v[58:59], v[66:67]
	s_nop 0
	v_cvt_pk_fp8_f32 v17, v52, v53
	v_cvt_pk_bf16_f32 v56, v52, v53
	v_pk_fma_f32 v[50:51], v[50:51], v[60:61], v[68:69]
	v_lshlrev_b32_e32 v58, 16, v56
	v_and_b32_e32 v59, 0xffff0000, v56
	v_cvt_pk_bf16_f32 v57, v50, v51
	v_pk_add_f32 v[58:59], v[52:53], v[58:59] neg_lo:[0,1] neg_hi:[0,1]
	v_cvt_pk_fp8_f32 v17, v50, v51 op_sel:[0,0,1]
	global_store_dwordx2 v[62:63], v[56:57], off offset:3584
	v_cvt_pk_bf16_f32 v56, v58, v59
	v_lshlrev_b32_e32 v58, 16, v57
	v_and_b32_e32 v59, 0xffff0000, v57
	v_pk_add_f32 v[58:59], v[50:51], v[58:59] neg_lo:[0,1] neg_hi:[0,1]
	v_lshlrev_b32_e32 v66, 16, v46
	v_cvt_pk_bf16_f32 v57, v58, v59
	global_store_dwordx2 v[64:65], v[56:57], off offset:3584
	global_store_dword v[54:55], v17, off offset:1792
	v_add_f32_e32 v17, v70, v71
	v_and_b32_e32 v67, 0xffff0000, v46
	v_lshlrev_b32_e32 v68, 16, v47
	v_and_b32_e32 v69, 0xffff0000, v47
	v_add_f32_e32 v17, v17, v19
	v_add_f32_e32 v19, v66, v67
	v_add_f32_e32 v21, v68, v69
	v_add_f32_e32 v17, 0, v17
	v_add_f32_e32 v19, v19, v21
	v_lshlrev_b32_e32 v62, 16, v44
	v_and_b32_e32 v63, 0xffff0000, v44
	v_lshlrev_b32_e32 v64, 16, v45
	v_and_b32_e32 v65, 0xffff0000, v45
	v_add_f32_e32 v17, v17, v19
	v_add_f32_e32 v19, v62, v63
	v_add_f32_e32 v21, v64, v65
	v_add_f32_e32 v19, v19, v21
	v_lshlrev_b32_e32 v58, 16, v42
	v_and_b32_e32 v59, 0xffff0000, v42
	v_lshlrev_b32_e32 v60, 16, v43
	v_and_b32_e32 v61, 0xffff0000, v43
	v_add_f32_e32 v17, v17, v19
	v_add_f32_e32 v19, v58, v59
	v_add_f32_e32 v21, v60, v61
	v_add_f32_e32 v19, v19, v21
	v_lshlrev_b32_e32 v54, 16, v40
	v_and_b32_e32 v55, 0xffff0000, v40
	v_lshlrev_b32_e32 v56, 16, v41
	v_and_b32_e32 v57, 0xffff0000, v41
	v_add_f32_e32 v17, v17, v19
	v_add_f32_e32 v19, v54, v55
	v_add_f32_e32 v21, v56, v57
	v_add_f32_e32 v19, v19, v21
	v_lshlrev_b32_e32 v50, 16, v38
	v_and_b32_e32 v51, 0xffff0000, v38
	v_lshlrev_b32_e32 v52, 16, v39
	v_and_b32_e32 v53, 0xffff0000, v39
	v_add_f32_e32 v17, v17, v19
	v_add_f32_e32 v19, v50, v51
	v_add_f32_e32 v21, v52, v53
	v_add_f32_e32 v19, v19, v21
	v_lshlrev_b32_e32 v46, 16, v34
	v_and_b32_e32 v47, 0xffff0000, v34
	v_add_f32_e32 v17, v17, v19
	v_add_f32_e32 v19, v46, v47
	v_add_f32_e32 v21, v48, v49
	v_add_f32_e32 v19, v19, v21
	v_lshlrev_b32_e32 v34, 16, v36
	v_lshlrev_b32_e32 v36, 16, v37
	v_and_b32_e32 v37, 0xffff0000, v37
	v_add_f32_e32 v17, v17, v19
	v_add_f32_e32 v19, v34, v35
	v_add_f32_e32 v21, v36, v37
	v_add_f32_e32 v19, v19, v21
	v_add_f32_e32 v17, v17, v19
	s_nop 1
; __device__ __forceinline__ unsigned pk2(float lo, float hi) { return hw_pk_bf16(lo, hi); }
; __device__ __forceinline__ unsigned pk4_fp8(float a, float b, float c, float d) { int w = __builtin_amdgcn_cvt_pk_fp8_f32(a, b, 0, false); w = __builtin_amdgcn_cvt_pk_fp8_f32(c, d, w, true); return (unsigned)w; }
; __device__ __forceinline__ void ln_router_tile(const Frame& F, const bf16* yf, const float* g1, const float* b1, bf16* x1b, bf16* x1l, unsigned char* x1q, const bf16* __restrict__ rthi, const bf16* __restrict__ rtlo, ...
;     ...
;         const float mean = wave_sum(s) * (1.0f / D); float s2 = 0.f;
; #pragma unroll
;         for (int j = 0; j < 8; ++j) { v[j] = v[j] - mean; s2 += (v[j].x * v[j].x + v[j].y * v[j].y) + (v[j].z * v[j].z + v[j].w * v[j].w); }
;         const float rstd = rsqrtf(wave_sum(s2) * (1.0f / D) + EPS);
; #pragma unroll
;         for (int j = 0; j < 8; ++j) { const int c = 4 * lane + 256 * j; const f32x4 gg = *(const f32x4*)(g1 + c), bb = *(const f32x4*)(b1 + c);
;             const f32x4 o = v[j] * rstd * gg + bb;
;             u32x2 wh; wh.x = pk2(o.x, o.y); wh.y = pk2(o.z, o.w); *(u32x2*)(x1b + (size_t)t * D + c) = wh;
;             u32x2 wl; wl.x = pk2(o.x - bflo(wh.x), o.y - bfhi(wh.x)); wl.y = pk2(o.z - bflo(wh.y), o.w - bfhi(wh.y)); *(u32x2*)(x1l + (size_t)t * D + c) = wl;
;             if (x1q) *(unsigned*)(x1q + (size_t)t * D + c) = pk4_fp8(o.x, o.y, o.z, o.w); }
	v_add_f32_dpp v17, v17, v17 quad_perm:[1,0,3,2] row_mask:0xf bank_mask:0xf bound_ctrl:1
	s_nop 1
	v_add_f32_dpp v17, v17, v17 quad_perm:[2,3,0,1] row_mask:0xf bank_mask:0xf bound_ctrl:1
	s_nop 1
	v_add_f32_dpp v17, v17, v17 row_half_mirror row_mask:0xf bank_mask:0xf bound_ctrl:1
	s_nop 1
	v_add_f32_dpp v17, v17, v17 row_mirror row_mask:0xf bank_mask:0xf bound_ctrl:1
	v_mov_b32_e32 v19, v17
	s_nop 1
	v_permlane32_swap_b32 v19, v17
	s_nop 0
	v_add_f32_e32 v17, v19, v17
	s_nop 0
	v_readlane_b32 s5, v17, 16
	v_readlane_b32 s4, v17, 0
	s_nop 0
	v_mov_b32_e32 v17, s5
	v_add_f32_e32 v17, s4, v17
	v_fmac_f32_e32 v77, 0xba000000, v17
	v_fmac_f32_e32 v71, 0xba000000, v17
	v_fmac_f32_e32 v76, 0xba000000, v17
	v_fmac_f32_e32 v70, 0xba000000, v17
	v_mul_f32_e32 v19, v71, v71
	v_mul_f32_e32 v21, v77, v77
	v_fmac_f32_e32 v19, v70, v70
	v_fmac_f32_e32 v21, v76, v76
	v_fmac_f32_e32 v69, 0xba000000, v17
	v_fmac_f32_e32 v67, 0xba000000, v17
	v_add_f32_e32 v19, v19, v21
	v_fmac_f32_e32 v68, 0xba000000, v17
	v_fmac_f32_e32 v66, 0xba000000, v17
	v_mul_f32_e32 v21, v67, v67
	v_mul_f32_e32 v38, v69, v69
	v_fmac_f32_e32 v21, v66, v66
	v_fmac_f32_e32 v38, v68, v68
	v_add_f32_e32 v21, v21, v38
	v_fmac_f32_e32 v65, 0xba000000, v17
	v_fmac_f32_e32 v63, 0xba000000, v17
	v_add_f32_e32 v19, v19, v21
	v_fmac_f32_e32 v64, 0xba000000, v17
	v_fmac_f32_e32 v62, 0xba000000, v17
	v_mul_f32_e32 v21, v63, v63
	v_mul_f32_e32 v38, v65, v65
	v_fmac_f32_e32 v21, v62, v62
	v_fmac_f32_e32 v38, v64, v64
	v_add_f32_e32 v21, v21, v38
	v_fmac_f32_e32 v61, 0xba000000, v17
	v_fmac_f32_e32 v59, 0xba000000, v17
	v_add_f32_e32 v19, v21, v19
	v_fmac_f32_e32 v60, 0xba000000, v17
	v_fmac_f32_e32 v58, 0xba000000, v17
	v_mul_f32_e32 v21, v59, v59
	v_mul_f32_e32 v38, v61, v61
	v_fmac_f32_e32 v21, v58, v58
	v_fmac_f32_e32 v38, v60, v60
	v_add_f32_e32 v21, v21, v38
	v_fmac_f32_e32 v57, 0xba000000, v17
	v_fmac_f32_e32 v55, 0xba000000, v17
	v_add_f32_e32 v19, v21, v19
	v_fmac_f32_e32 v56, 0xba000000, v17
	v_fmac_f32_e32 v54, 0xba000000, v17
	v_mul_f32_e32 v21, v55, v55
	v_mul_f32_e32 v38, v57, v57
	v_fmac_f32_e32 v21, v54, v54
	v_fmac_f32_e32 v38, v56, v56
	v_add_f32_e32 v21, v21, v38
	v_fmac_f32_e32 v53, 0xba000000, v17
	v_fmac_f32_e32 v51, 0xba000000, v17
	v_add_f32_e32 v19, v21, v19
	v_fmac_f32_e32 v52, 0xba000000, v17
	v_fmac_f32_e32 v50, 0xba000000, v17
	v_mul_f32_e32 v21, v51, v51
	v_mul_f32_e32 v38, v53, v53
	v_fmac_f32_e32 v21, v50, v50
	v_fmac_f32_e32 v38, v52, v52
	v_add_f32_e32 v21, v21, v38
	v_fmac_f32_e32 v49, 0xba000000, v17
	v_fmac_f32_e32 v47, 0xba000000, v17
	v_add_f32_e32 v19, v21, v19
	v_fmac_f32_e32 v48, 0xba000000, v17
	v_fmac_f32_e32 v46, 0xba000000, v17
	v_mul_f32_e32 v21, v47, v47
	v_mul_f32_e32 v38, v49, v49
	v_fmac_f32_e32 v21, v46, v46
	v_fmac_f32_e32 v38, v48, v48
	v_add_f32_e32 v21, v21, v38
	v_fmac_f32_e32 v37, 0xba000000, v17
	v_fmac_f32_e32 v35, 0xba000000, v17
	v_add_f32_e32 v19, v21, v19
	v_fmac_f32_e32 v36, 0xba000000, v17
	v_fmac_f32_e32 v34, 0xba000000, v17
	v_mul_f32_e32 v17, v35, v35
	v_mul_f32_e32 v21, v37, v37
	v_fmac_f32_e32 v17, v34, v34
	v_fmac_f32_e32 v21, v36, v36
	v_add_f32_e32 v17, v17, v21
	v_add_f32_e32 v17, v17, v19
	s_nop 1
	v_add_f32_dpp v17, v17, v17 quad_perm:[1,0,3,2] row_mask:0xf bank_mask:0xf bound_ctrl:1
	s_nop 1
	v_add_f32_dpp v17, v17, v17 quad_perm:[2,3,0,1] row_mask:0xf bank_mask:0xf bound_ctrl:1
	s_nop 1
	v_add_f32_dpp v17, v17, v17 row_half_mirror row_mask:0xf bank_mask:0xf bound_ctrl:1
	s_nop 1
	v_add_f32_dpp v17, v17, v17 row_mirror row_mask:0xf bank_mask:0xf bound_ctrl:1
	v_mov_b32_e32 v19, v17
	s_nop 1
	v_permlane32_swap_b32 v17, v19
	v_mov_b64_e32 v[42:43], v[128:129]
	v_mov_b64_e32 v[44:45], v[130:131]
	v_mov_b64_e32 v[72:73], v[160:161]
	v_mov_b64_e32 v[74:75], v[162:163]
	v_add_f32_e32 v17, v17, v19
	s_nop 0
	v_readlane_b32 s5, v17, 16
	v_readlane_b32 s4, v17, 0
	s_nop 0
	v_mov_b32_e32 v17, s5
	v_add_f32_e32 v17, s4, v17
	v_fmamk_f32 v17, v17, 0x3a000000, v194
	v_cmp_gt_f32_e64 s[36:37], s26, v17
	v_mul_f32_e32 v19, 0x4b800000, v17
	s_mov_b64 s[4:5], 0
	v_cndmask_b32_e64 v17, v17, v19, s[36:37]
	v_rsq_f32_e32 v17, v17
	s_nop 0
	v_mul_f32_e32 v19, 0x45800000, v17
	v_cndmask_b32_e64 v40, v17, v19, s[36:37]
	v_pk_mul_f32 v[38:39], v[70:71], v[40:41] op_sel_hi:[1,0]
	v_mov_b32_e32 v17, v193
	v_pk_mul_f32 v[70:71], v[76:77], v[40:41] op_sel_hi:[1,0]
	v_pk_mul_f32 v[66:67], v[66:67], v[40:41] op_sel_hi:[1,0]
	v_pk_mul_f32 v[68:69], v[68:69], v[40:41] op_sel_hi:[1,0]
	v_pk_mul_f32 v[62:63], v[62:63], v[40:41] op_sel_hi:[1,0]
	v_pk_mul_f32 v[64:65], v[64:65], v[40:41] op_sel_hi:[1,0]
	v_pk_mul_f32 v[58:59], v[58:59], v[40:41] op_sel_hi:[1,0]
	v_pk_mul_f32 v[60:61], v[60:61], v[40:41] op_sel_hi:[1,0]
	v_pk_mul_f32 v[54:55], v[54:55], v[40:41] op_sel_hi:[1,0]
	v_pk_mul_f32 v[56:57], v[56:57], v[40:41] op_sel_hi:[1,0]
	v_pk_mul_f32 v[50:51], v[50:51], v[40:41] op_sel_hi:[1,0]
	v_pk_mul_f32 v[52:53], v[52:53], v[40:41] op_sel_hi:[1,0]
	v_pk_mul_f32 v[46:47], v[46:47], v[40:41] op_sel_hi:[1,0]
	v_pk_mul_f32 v[48:49], v[48:49], v[40:41] op_sel_hi:[1,0]
	v_pk_mul_f32 v[34:35], v[34:35], v[40:41] op_sel_hi:[1,0]
	v_pk_mul_f32 v[36:37], v[36:37], v[40:41] op_sel_hi:[1,0]
	v_pk_fma_f32 v[72:73], v[42:43], v[38:39], v[72:73]
	s_nop 0
	v_cvt_pk_fp8_f32 v17, v72, v73
	v_cvt_pk_bf16_f32 v38, v72, v73
	v_pk_fma_f32 v[70:71], v[44:45], v[70:71], v[74:75]
	v_lshlrev_b32_e32 v44, 16, v38
	v_and_b32_e32 v45, 0xffff0000, v38
	v_cvt_pk_bf16_f32 v39, v70, v71
	v_lshl_add_u64 v[42:43], v[28:29], 0, s[38:39]
	v_pk_add_f32 v[44:45], v[72:73], v[44:45] neg_lo:[0,1] neg_hi:[0,1]
	global_store_dwordx2 v[42:43], v[38:39], off
	v_cvt_pk_bf16_f32 v38, v44, v45
; __device__ __forceinline__ unsigned pk2(float lo, float hi) { return hw_pk_bf16(lo, hi); }
; __device__ __forceinline__ unsigned pk4_fp8(float a, float b, float c, float d) { int w = __builtin_amdgcn_cvt_pk_fp8_f32(a, b, 0, false); w = __builtin_amdgcn_cvt_pk_fp8_f32(c, d, w, true); return (unsigned)w; }
; __device__ __forceinline__ void ln_router_tile(const Frame& F, const bf16* yf, const float* g1, const float* b1, bf16* x1b, bf16* x1l, unsigned char* x1q, const bf16* __restrict__ rthi, const bf16* __restrict__ rtlo, ...
;     ...
; #pragma unroll
;         for (int j = 0; j < 8; ++j) { const int c = 4 * lane + 256 * j; const f32x4 gg = *(const f32x4*)(g1 + c), bb = *(const f32x4*)(b1 + c);
;             const f32x4 o = v[j] * rstd * gg + bb;
;             u32x2 wh; wh.x = pk2(o.x, o.y); wh.y = pk2(o.z, o.w); *(u32x2*)(x1b + (size_t)t * D + c) = wh;
;             u32x2 wl; wl.x = pk2(o.x - bflo(wh.x), o.y - bfhi(wh.x)); wl.y = pk2(o.z - bflo(wh.y), o.w - bfhi(wh.y)); *(u32x2*)(x1l + (size_t)t * D + c) = wl;
;             if (x1q) *(unsigned*)(x1q + (size_t)t * D + c) = pk4_fp8(o.x, o.y, o.z, o.w); }
	v_lshlrev_b32_e32 v44, 16, v39
	v_and_b32_e32 v45, 0xffff0000, v39
	v_cvt_pk_fp8_f32 v17, v70, v71 op_sel:[0,0,1]
	v_pk_add_f32 v[44:45], v[70:71], v[44:45] neg_lo:[0,1] neg_hi:[0,1]
	s_nop 0
	v_cvt_pk_bf16_f32 v39, v44, v45
	v_lshl_add_u64 v[44:45], v[30:31], 0, s[38:39]
	global_store_dwordx2 v[44:45], v[38:39], off
	v_lshl_add_u64 v[38:39], v[32:33], 0, s[42:43]
	global_store_dword v[38:39], v17, off
	v_mov_b64_e32 v[70:71], v[132:133]
	v_mov_b64_e32 v[72:73], v[134:135]
	v_mov_b64_e32 v[74:75], v[164:165]
	v_mov_b64_e32 v[76:77], v[166:167]
	v_mov_b32_e32 v17, v193
	v_pk_fma_f32 v[66:67], v[70:71], v[66:67], v[74:75]
	s_nop 0
	v_cvt_pk_fp8_f32 v17, v66, v67
	v_cvt_pk_bf16_f32 v70, v66, v67
	v_pk_fma_f32 v[68:69], v[72:73], v[68:69], v[76:77]
	v_lshlrev_b32_e32 v72, 16, v70
	v_and_b32_e32 v73, 0xffff0000, v70
	v_cvt_pk_bf16_f32 v71, v68, v69
	v_pk_add_f32 v[72:73], v[66:67], v[72:73] neg_lo:[0,1] neg_hi:[0,1]
	v_cvt_pk_fp8_f32 v17, v68, v69 op_sel:[0,0,1]
	global_store_dwordx2 v[42:43], v[70:71], off offset:512
	v_cvt_pk_bf16_f32 v70, v72, v73
	v_lshlrev_b32_e32 v72, 16, v71
	v_and_b32_e32 v73, 0xffff0000, v71
	v_pk_add_f32 v[72:73], v[68:69], v[72:73] neg_lo:[0,1] neg_hi:[0,1]
	s_nop 0
	v_cvt_pk_bf16_f32 v71, v72, v73
	global_store_dwordx2 v[44:45], v[70:71], off offset:512
	global_store_dword v[38:39], v17, off offset:256
	v_mov_b64_e32 v[66:67], v[136:137]
	v_mov_b64_e32 v[68:69], v[138:139]
	s_nop 0
	v_mov_b64_e32 v[70:71], v[168:169]
	v_mov_b64_e32 v[72:73], v[170:171]
	v_mov_b32_e32 v17, v193
	v_pk_fma_f32 v[62:63], v[62:63], v[66:67], v[70:71]
	s_nop 0
	v_cvt_pk_fp8_f32 v17, v62, v63
	v_cvt_pk_bf16_f32 v66, v62, v63
	v_pk_fma_f32 v[64:65], v[64:65], v[68:69], v[72:73]
	v_lshlrev_b32_e32 v68, 16, v66
	v_and_b32_e32 v69, 0xffff0000, v66
	v_cvt_pk_bf16_f32 v67, v64, v65
	v_pk_add_f32 v[68:69], v[62:63], v[68:69] neg_lo:[0,1] neg_hi:[0,1]
	v_cvt_pk_fp8_f32 v17, v64, v65 op_sel:[0,0,1]
	global_store_dwordx2 v[42:43], v[66:67], off offset:1024
	v_cvt_pk_bf16_f32 v66, v68, v69
	v_lshlrev_b32_e32 v68, 16, v67
	v_and_b32_e32 v69, 0xffff0000, v67
	v_pk_add_f32 v[68:69], v[64:65], v[68:69] neg_lo:[0,1] neg_hi:[0,1]
	s_nop 0
	v_cvt_pk_bf16_f32 v67, v68, v69
	global_store_dwordx2 v[44:45], v[66:67], off offset:1024
	global_store_dword v[38:39], v17, off offset:512
	v_mov_b64_e32 v[62:63], v[140:141]
	v_mov_b64_e32 v[64:65], v[142:143]
	s_nop 0
	v_mov_b64_e32 v[66:67], v[172:173]
	v_mov_b64_e32 v[68:69], v[174:175]
	v_mov_b32_e32 v17, v193
	v_pk_fma_f32 v[58:59], v[58:59], v[62:63], v[66:67]
	s_nop 0
	v_cvt_pk_fp8_f32 v17, v58, v59
	v_cvt_pk_bf16_f32 v62, v58, v59
	v_pk_fma_f32 v[60:61], v[60:61], v[64:65], v[68:69]
	v_lshlrev_b32_e32 v64, 16, v62
	v_and_b32_e32 v65, 0xffff0000, v62
	v_cvt_pk_bf16_f32 v63, v60, v61
	v_pk_add_f32 v[64:65], v[58:59], v[64:65] neg_lo:[0,1] neg_hi:[0,1]
	v_cvt_pk_fp8_f32 v17, v60, v61 op_sel:[0,0,1]
	global_store_dwordx2 v[42:43], v[62:63], off offset:1536
	v_cvt_pk_bf16_f32 v62, v64, v65
	v_lshlrev_b32_e32 v64, 16, v63
	v_and_b32_e32 v65, 0xffff0000, v63
	v_pk_add_f32 v[64:65], v[60:61], v[64:65] neg_lo:[0,1] neg_hi:[0,1]
	s_nop 0
	v_cvt_pk_bf16_f32 v63, v64, v65
	global_store_dwordx2 v[44:45], v[62:63], off offset:1536
	global_store_dword v[38:39], v17, off offset:768
	v_mov_b64_e32 v[58:59], v[144:145]
	v_mov_b64_e32 v[60:61], v[146:147]
	s_nop 0
	v_mov_b64_e32 v[62:63], v[176:177]
	v_mov_b64_e32 v[64:65], v[178:179]
	v_mov_b32_e32 v17, v193
	v_pk_fma_f32 v[54:55], v[54:55], v[58:59], v[62:63]
	s_nop 0
	v_cvt_pk_fp8_f32 v17, v54, v55
	v_cvt_pk_bf16_f32 v58, v54, v55
	v_pk_fma_f32 v[56:57], v[56:57], v[60:61], v[64:65]
	v_lshlrev_b32_e32 v60, 16, v58
	v_and_b32_e32 v61, 0xffff0000, v58
	v_cvt_pk_bf16_f32 v59, v56, v57
	v_pk_add_f32 v[60:61], v[54:55], v[60:61] neg_lo:[0,1] neg_hi:[0,1]
	v_cvt_pk_fp8_f32 v17, v56, v57 op_sel:[0,0,1]
	global_store_dwordx2 v[42:43], v[58:59], off offset:2048
	v_cvt_pk_bf16_f32 v58, v60, v61
	v_lshlrev_b32_e32 v60, 16, v59
	v_and_b32_e32 v61, 0xffff0000, v59
	v_pk_add_f32 v[60:61], v[56:57], v[60:61] neg_lo:[0,1] neg_hi:[0,1]
	s_nop 0
	v_cvt_pk_bf16_f32 v59, v60, v61
	global_store_dwordx2 v[44:45], v[58:59], off offset:2048
	global_store_dword v[38:39], v17, off offset:1024
	v_mov_b64_e32 v[54:55], v[148:149]
	v_mov_b64_e32 v[56:57], v[150:151]
	s_nop 0
	v_mov_b64_e32 v[58:59], v[180:181]
	v_mov_b64_e32 v[60:61], v[182:183]
	v_mov_b32_e32 v17, v193
	v_pk_fma_f32 v[50:51], v[50:51], v[54:55], v[58:59]
	s_nop 0
	v_cvt_pk_fp8_f32 v17, v50, v51
	v_cvt_pk_bf16_f32 v54, v50, v51
	v_pk_fma_f32 v[52:53], v[52:53], v[56:57], v[60:61]
	v_lshlrev_b32_e32 v56, 16, v54
	v_and_b32_e32 v57, 0xffff0000, v54
	v_cvt_pk_bf16_f32 v55, v52, v53
	v_pk_add_f32 v[56:57], v[50:51], v[56:57] neg_lo:[0,1] neg_hi:[0,1]
	v_cvt_pk_fp8_f32 v17, v52, v53 op_sel:[0,0,1]
	global_store_dwordx2 v[42:43], v[54:55], off offset:2560
	v_cvt_pk_bf16_f32 v54, v56, v57
	v_lshlrev_b32_e32 v56, 16, v55
	v_and_b32_e32 v57, 0xffff0000, v55
	v_pk_add_f32 v[56:57], v[52:53], v[56:57] neg_lo:[0,1] neg_hi:[0,1]
	s_nop 0
	v_cvt_pk_bf16_f32 v55, v56, v57
	global_store_dwordx2 v[44:45], v[54:55], off offset:2560
	global_store_dword v[38:39], v17, off offset:1280
	v_mov_b64_e32 v[50:51], v[152:153]
	v_mov_b64_e32 v[52:53], v[154:155]
	s_nop 0
	v_mov_b64_e32 v[54:55], v[184:185]
	v_mov_b64_e32 v[56:57], v[186:187]
	v_mov_b32_e32 v17, v193
	v_pk_fma_f32 v[46:47], v[46:47], v[50:51], v[54:55]
	s_nop 0
	v_cvt_pk_fp8_f32 v17, v46, v47
; __device__ __forceinline__ unsigned pk2(float lo, float hi) { return hw_pk_bf16(lo, hi); }
; __device__ __forceinline__ unsigned pk4_fp8(float a, float b, float c, float d) { int w = __builtin_amdgcn_cvt_pk_fp8_f32(a, b, 0, false); w = __builtin_amdgcn_cvt_pk_fp8_f32(c, d, w, true); return (unsigned)w; }
; #define RT_DMA(c) do { _Pragma("unroll") for (int i = 0; i < 4; ++i) \
;           __builtin_amdgcn_global_load_lds((const unsigned*)(gp[i] + 64 * (c)), (LAS unsigned*)(lds + ((c) & 3) * 32768 + dbase + i * 1024), 16, 0, 0); } while (0)
; __device__ __forceinline__ void ln_router_tile(const Frame& F, const bf16* yf, const float* g1, const float* b1, bf16* x1b, bf16* x1l, unsigned char* x1q, const bf16* __restrict__ rthi, const bf16* __restrict__ rtlo, ...
;     ...
; #pragma unroll
;         for (int j = 0; j < 8; ++j) { const int c = 4 * lane + 256 * j; const f32x4 gg = *(const f32x4*)(g1 + c), bb = *(const f32x4*)(b1 + c);
;             const f32x4 o = v[j] * rstd * gg + bb;
;             u32x2 wh; wh.x = pk2(o.x, o.y); wh.y = pk2(o.z, o.w); *(u32x2*)(x1b + (size_t)t * D + c) = wh;
;             u32x2 wl; wl.x = pk2(o.x - bflo(wh.x), o.y - bfhi(wh.x)); wl.y = pk2(o.z - bflo(wh.y), o.w - bfhi(wh.y)); *(u32x2*)(x1l + (size_t)t * D + c) = wl;
;             if (x1q) *(unsigned*)(x1q + (size_t)t * D + c) = pk4_fp8(o.x, o.y, o.z, o.w); }
;     ...
;     { const int tt = w >> 2, et = (w >> 1) & 1, kh = w & 1;
;       asm volatile("" ::: "memory");
;       f32x16 acc = (f32x16){};
;       const int mm = w >> 1; const bf16* mbase = (mm == 0) ? x1b + (size_t)t0 * D : (mm == 1) ? x1l + (size_t)t0 * D : (mm == 2) ? rthi : rtlo;
;       const bf16* gp[4];
; #pragma unroll
;       for (int i = 0; i < 4; ++i) { const int row = 32 * (w & 1) + 8 * i + (lane >> 3); gp[i] = mbase + (size_t)row * D + 8 * ((lane & 7) ^ ((row >> 1) & 7)); }
;       const unsigned dbase = (unsigned)mm * 8192u + (unsigned)(w & 1) * 4096u;
;     ...
;       RT_DMA(0); RT_DMA(1); RT_DMA(2);
;       const int ra = 32 * tt + r32, rb = 32 * et + r32, sa = (ra >> 1) & 7, sb = (rb >> 1) & 7;
	v_cvt_pk_bf16_f32 v50, v46, v47
	v_pk_fma_f32 v[48:49], v[48:49], v[52:53], v[56:57]
	v_lshlrev_b32_e32 v52, 16, v50
	v_and_b32_e32 v53, 0xffff0000, v50
	v_cvt_pk_bf16_f32 v51, v48, v49
	v_pk_add_f32 v[52:53], v[46:47], v[52:53] neg_lo:[0,1] neg_hi:[0,1]
	v_cvt_pk_fp8_f32 v17, v48, v49 op_sel:[0,0,1]
	global_store_dwordx2 v[42:43], v[50:51], off offset:3072
	v_cvt_pk_bf16_f32 v50, v52, v53
	v_lshlrev_b32_e32 v52, 16, v51
	v_and_b32_e32 v53, 0xffff0000, v51
	v_pk_add_f32 v[52:53], v[48:49], v[52:53] neg_lo:[0,1] neg_hi:[0,1]
	s_nop 0
	v_cvt_pk_bf16_f32 v51, v52, v53
	global_store_dwordx2 v[44:45], v[50:51], off offset:3072
	global_store_dword v[38:39], v17, off offset:1536
	v_mov_b64_e32 v[46:47], v[156:157]
	v_mov_b64_e32 v[48:49], v[158:159]
	s_nop 0
	v_mov_b64_e32 v[50:51], v[188:189]
	v_mov_b64_e32 v[52:53], v[190:191]
	v_mov_b32_e32 v17, v193
	v_pk_fma_f32 v[34:35], v[34:35], v[46:47], v[50:51]
	s_nop 0
	v_cvt_pk_fp8_f32 v17, v34, v35
	v_pk_fma_f32 v[36:37], v[36:37], v[48:49], v[52:53]
	v_cvt_pk_bf16_f32 v40, v34, v35
	v_cvt_pk_bf16_f32 v41, v36, v37
	global_store_dwordx2 v[42:43], v[40:41], off offset:3584
	v_lshlrev_b32_e32 v42, 16, v40
	v_and_b32_e32 v43, 0xffff0000, v40
	v_pk_add_f32 v[42:43], v[34:35], v[42:43] neg_lo:[0,1] neg_hi:[0,1]
	v_cvt_pk_fp8_f32 v17, v36, v37 op_sel:[0,0,1]
	v_cvt_pk_bf16_f32 v40, v42, v43
	v_lshlrev_b32_e32 v42, 16, v41
	v_and_b32_e32 v43, 0xffff0000, v41
	v_pk_add_f32 v[42:43], v[36:37], v[42:43] neg_lo:[0,1] neg_hi:[0,1]
	s_nop 0
	v_cvt_pk_bf16_f32 v41, v42, v43
	global_store_dwordx2 v[44:45], v[40:41], off offset:3584
	global_store_dword v[38:39], v17, off offset:1792
	s_cbranch_vccz .LBB0_791
	s_ashr_i32 s97, s96, 31
	s_lshl_b64 s[4:5], s[96:97], 12
	s_add_u32 s6, s48, s4
	s_addc_u32 s7, s49, s5
	s_add_u32 s8, s46, s4
	s_addc_u32 s9, s47, s5
	v_lshrrev_b32_e32 v17, 3, v20
	s_and_b64 s[4:5], s[88:89], exec
	v_lshrrev_b32_e32 v8, 4, v20
	v_or_b32_e32 v6, s53, v17
	s_cselect_b32 s6, s6, s35
	s_cselect_b32 s7, s7, s30
	s_and_b64 s[4:5], s[86:87], exec
	v_xor_b32_e32 v2, v8, v16
	s_cselect_b32 s5, s9, s7
	s_cselect_b32 s4, s8, s6
	v_lshlrev_b32_e32 v192, 12, v6
	v_lshlrev_b32_e32 v2, 4, v2
	v_or_b32_e32 v4, 8, v6
	v_lshl_add_u64 v[0:1], s[4:5], 0, v[192:193]
	v_and_b32_e32 v192, 0x70, v2
	v_lshrrev_b32_e32 v9, 1, v4
	v_lshl_add_u64 v[0:1], v[0:1], 0, v[192:193]
	v_lshlrev_b32_e32 v192, 12, v4
	v_xor_b32_e32 v4, v9, v16
	v_lshlrev_b32_e32 v4, 4, v4
	v_lshl_add_u64 v[2:3], s[4:5], 0, v[192:193]
	v_and_b32_e32 v192, 0x70, v4
	v_or_b32_e32 v10, 24, v6
	v_lshl_add_u64 v[2:3], v[2:3], 0, v[192:193]
	v_lshlrev_b32_e32 v192, 12, v10
	v_lshrrev_b32_e32 v10, 1, v10
	s_mov_b32 m0, s2
	s_barrier
	v_xor_b32_e32 v11, v10, v16
	s_mov_b64 s[6:7], 0x10000
	v_lshlrev_b32_e32 v11, 4, v11
	global_load_lds_dwordx4 v[0:1], off
	s_add_i32 m0, s2, 0x400
	v_lshl_add_u64 v[4:5], v[0:1], 0, s[6:7]
	v_lshl_add_u64 v[6:7], s[4:5], 0, v[192:193]
	v_and_b32_e32 v192, 0x70, v11
	global_load_lds_dwordx4 v[2:3], off
	s_add_i32 m0, s2, 0x800
	v_lshl_add_u64 v[6:7], v[6:7], 0, v[192:193]
	global_load_lds_dwordx4 v[4:5], off
	s_add_i32 m0, s2, 0xc00
	v_lshl_add_u64 v[4:5], v[0:1], 0, s[62:63]
	global_load_lds_dwordx4 v[6:7], off
	s_add_i32 m0, s2, 0x8000
	s_mov_b64 s[6:7], 0x10080
	global_load_lds_dwordx4 v[4:5], off
	v_lshl_add_u64 v[4:5], v[2:3], 0, s[62:63]
	s_add_i32 m0, s2, 0x8400
	v_lshl_add_u64 v[2:3], v[2:3], 0, s[64:65]
	global_load_lds_dwordx4 v[4:5], off
	v_lshl_add_u64 v[4:5], v[0:1], 0, s[6:7]
	s_add_i32 m0, s2, 0x8800
	s_mov_b64 s[6:7], 0x10100
	global_load_lds_dwordx4 v[4:5], off
	v_lshl_add_u64 v[4:5], v[6:7], 0, s[62:63]
	s_add_i32 m0, s2, 0x8c00
	v_and_b32_e32 v21, 31, v16
	global_load_lds_dwordx4 v[4:5], off
	v_lshl_add_u64 v[4:5], v[0:1], 0, s[64:65]
	s_add_i32 m0, s2, 0x10000
	v_lshl_add_u64 v[0:1], v[0:1], 0, s[6:7]
	global_load_lds_dwordx4 v[4:5], off
	s_add_i32 m0, s2, 0x10400
	v_lshrrev_b32_e32 v19, 5, v20
	global_load_lds_dwordx4 v[2:3], off
	s_add_i32 m0, s2, 0x10800
	v_or_b32_e32 v2, s24, v19
	global_load_lds_dwordx4 v[0:1], off
	v_lshl_add_u64 v[0:1], v[6:7], 0, s[64:65]
	s_add_i32 m0, s2, 0x10c00
	s_mov_b32 s8, 0
	global_load_lds_dwordx4 v[0:1], off
	v_or_b32_e32 v0, s56, v21
	v_bfe_u32 v1, v16, 1, 3
	v_lshlrev_b32_e32 v28, 7, v0
	v_or_b32_e32 v0, s57, v21
	v_lshlrev_b32_e32 v29, 7, v0
	v_bitop3_b32 v0, v19, v1, s24 bitop3:0x36
	v_lshlrev_b32_e32 v30, 4, v0
	v_bitop3_b32 v0, v2, v1, 2 bitop3:0x36
	v_lshlrev_b32_e32 v31, 4, v0
	v_bitop3_b32 v0, v8, 7, v16 bitop3:0x48
	v_lshlrev_b32_e32 v192, 4, v0
	v_lshlrev_b32_e32 v0, 11, v17
	v_add_lshl_u32 v0, s60, v0, 1
	v_mov_b32_e32 v1, v193
	v_lshl_add_u64 v[0:1], v[192:193], 0, v[0:1]
	v_lshl_add_u64 v[22:23], s[4:5], 0, v[0:1]
	s_add_u32 s4, s4, 0x180
	v_bitop3_b32 v0, v9, 7, v16 bitop3:0x48
	v_add_lshl_u32 v1, s59, v17, 12
	s_addc_u32 s5, s5, 0
	v_lshl_or_b32 v192, v0, 4, v1
	v_bitop3_b32 v0, v10, 7, v16 bitop3:0x48
	v_add_lshl_u32 v1, s22, v17, 12
	v_lshl_add_u64 v[24:25], s[4:5], 0, v[192:193]
	v_lshl_or_b32 v192, v0, 4, v1
	v_mov_b32_e32 v0, 0
	v_lshl_add_u64 v[26:27], s[4:5], 0, v[192:193]
	s_mov_b32 s9, 0x18000
	s_mov_b64 s[4:5], 0
	v_mov_b32_e32 v1, v0
	v_mov_b32_e32 v2, v0
	v_mov_b32_e32 v3, v0
	v_mov_b32_e32 v4, v0
	v_mov_b32_e32 v5, v0
	v_mov_b32_e32 v6, v0
	v_mov_b32_e32 v7, v0
	v_mov_b32_e32 v8, v0
	v_mov_b32_e32 v9, v0
	v_mov_b32_e32 v10, v0
	v_mov_b32_e32 v11, v0
	v_mov_b32_e32 v12, v0
	v_mov_b32_e32 v13, v0
	v_mov_b32_e32 v14, v0
	v_mov_b32_e32 v15, v0
	s_branch .LBB0_794

; #define PG8_STAGE(bufoff, gbase, voff) do { _Pragma("unroll") for (int _i = 0; _i < 2; ++_i) \
;         __builtin_amdgcn_global_load_lds((const unsigned*)((const char*)(gbase) + (voff)[_i]), (LAS unsigned*)(lds + (bufoff) + ldsw + _i * 8192), 16, 0, 0); } while (0)
; #define PG8_LDA(dst, b, h) do { _Pragma("unroll") for (int m = 0; m < 4; ++m) _Pragma("unroll") for (int k = 0; k < 2; ++k) dst[m][k] = *(const LAS bf16x8*)(lds + PG8_SA(b, h) + aoff + m * 2048 + k * KOFF); } while (0)
; #define PG8_LDB(dst, b, h) do { _Pragma("unroll") for (int n = 0; n < 2; ++n) _Pragma("unroll") for (int k = 0; k < 2; ++k) dst[n][k] = *(const LAS bf16x8*)(lds + PG8_SB(b, h) + boff + n * 2048 + k * KOFF); } while (0)
; #define PG8_WAIT_V(n) asm volatile("s_waitcnt vmcnt(" #n ")" ::: "memory")
; #define PG8_WAIT_L(n) asm volatile("s_waitcnt lgkmcnt(" #n ")" ::: "memory")
; #define PG8_BAR __builtin_amdgcn_s_barrier()
; #define PG8_SCHED __builtin_amdgcn_sched_barrier(0)
; #define PG8_AOFF(u_, o0, o1) do { _Pragma("unroll") for (int _i = 0; _i < 2; ++_i) { const int r0 = (u_).pm * BM + Rr[_i], r1 = r0 + HALF; \
;         const int g0 = GATHER ? g.rowidx[r0] : r0, g1 = GATHER ? g.rowidx[r1] : r1; \
;         o0[_i] = (unsigned)g0 * (unsigned)K + (unsigned)Cc[_i]; o1[_i] = (unsigned)g1 * (unsigned)K + (unsigned)Cc[_i]; } } while (0)
; template <class Epi, class Sched, bool GATHER, bool FP8 = false, bool ALIGN = true>
; __device__ __forceinline__ void gemm_phase(LAS unsigned char* lds, int wave, const Gemm g, const Sched& S, const Epi& E) {
;     ...
;         for (int t = 0; t < nt; t += 2) {
;             const bool last = (t == nt - 2);
;             const char* a1 = Ab + (size_t)(t + 1) * kstep;
;             const char* a2 = last ? Ab : Ab + (size_t)(t + 2) * kstep; const char* b2 = last ? nB : cB + (size_t)(t + 2) * kstep;
;             const char* a3 = a2 + kstep; const char* b3 = b2 + kstep;
;             PG8_LDB(B0, 0, 0); PG8_LDB(B1, 0, 1); PG8_SCHED; PG8_LDA(At, 0, 0); PG8_STAGE(PG8_SA(1, 1), a1, ca1);
;             if (last && has_next) PG8_AOFF(nxt, ca0, ca1);
;             PG8_WAIT_V(8); PG8_WAIT_L(0); PG8_BAR; PG8_MMA(0, 0, At, B0); PG8_MMA(0, 1, At, B1); PG8_BAR; PG8_SCHED;
;             PG8_LDA(At, 0, 1); PG8_STAGE(PG8_SB(0, 0), b2, voffB0); PG8_STAGE(PG8_SB(0, 1), b2, voffB1); PG8_STAGE(PG8_SA(0, 0), a2, ca0);
.Lpeel_gu_b:
	s_waitcnt vmcnt(8)
	s_add_u32 s14, s10, 0x80
	s_waitcnt lgkmcnt(0)
	s_addc_u32 s15, s11, 0
	s_and_b64 s[12:13], s[12:13], exec
	v_mov_b32_e32 v217, v193
	s_cselect_b32 s13, s7, s15
	s_cselect_b32 s12, s6, s14
	s_cselect_b32 s15, s5, s82
	s_cselect_b32 s14, s9, s49
	s_barrier
	s_and_b64 vcc, exec, s[50:51]
	s_cbranch_vccz .Lgu_norow
	global_load_dword v240, v[218:219], off
	global_load_dword v241, v[218:219], off offset:512
	global_load_dword v242, v[220:221], off
	global_load_dword v243, v[220:221], off offset:512
.Lgu_norow:
	s_setprio 1
	s_waitcnt lgkmcnt(0)
	v_mfma_scale_f32_16x16x128_f8f6f4 v[188:191], v[16:23], v[56:63], 0, v252, v251 op_sel_hi:[0,0,0]
	v_mfma_scale_f32_16x16x128_f8f6f4 v[180:183], v[24:31], v[56:63], 0, v252, v251 op_sel_hi:[0,0,0]
	v_mfma_scale_f32_16x16x128_f8f6f4 v[172:175], v[16:23], v[48:55], 0, v252, v251 op_sel_hi:[0,0,0]
	v_mfma_scale_f32_16x16x128_f8f6f4 v[164:167], v[24:31], v[48:55], 0, v252, v251 op_sel_hi:[0,0,0]
	v_mfma_scale_f32_16x16x128_f8f6f4 v[156:159], v[16:23], v[40:47], 0, v252, v251 op_sel_hi:[0,0,0]
	v_mfma_scale_f32_16x16x128_f8f6f4 v[148:151], v[24:31], v[40:47], 0, v252, v251 op_sel_hi:[0,0,0]
	v_mfma_scale_f32_16x16x128_f8f6f4 v[140:143], v[16:23], v[32:39], 0, v252, v251 op_sel_hi:[0,0,0]
	v_mfma_scale_f32_16x16x128_f8f6f4 v[132:135], v[24:31], v[32:39], 0, v252, v251 op_sel_hi:[0,0,0]
	s_setprio 0
	s_setprio 1
	v_mfma_scale_f32_16x16x128_f8f6f4 v[184:187], v[0:7], v[56:63], 0, v252, v251 op_sel_hi:[0,0,0]
	v_mfma_scale_f32_16x16x128_f8f6f4 v[176:179], v[8:15], v[56:63], 0, v252, v251 op_sel_hi:[0,0,0]
	v_mfma_scale_f32_16x16x128_f8f6f4 v[168:171], v[0:7], v[48:55], 0, v252, v251 op_sel_hi:[0,0,0]
	v_mfma_scale_f32_16x16x128_f8f6f4 v[160:163], v[8:15], v[48:55], 0, v252, v251 op_sel_hi:[0,0,0]
	v_mfma_scale_f32_16x16x128_f8f6f4 v[152:155], v[0:7], v[40:47], 0, v252, v251 op_sel_hi:[0,0,0]
	v_mfma_scale_f32_16x16x128_f8f6f4 v[144:147], v[8:15], v[40:47], 0, v252, v251 op_sel_hi:[0,0,0]
	v_mfma_scale_f32_16x16x128_f8f6f4 v[136:139], v[0:7], v[32:39], 0, v252, v251 op_sel_hi:[0,0,0]
	v_mfma_scale_f32_16x16x128_f8f6f4 v[128:131], v[8:15], v[32:39], 0, v252, v251 op_sel_hi:[0,0,0]
	s_setprio 0
	s_barrier
	s_mov_b32 m0, s34
	v_lshl_add_u64 v[196:197], s[14:15], 0, v[204:205]
	ds_read_b128 v[32:35], v238 offset:16384
	ds_read_b128 v[36:39], v238 offset:17408
	ds_read_b128 v[40:43], v238 offset:18432
	ds_read_b128 v[44:47], v238 offset:19456
	ds_read_b128 v[48:51], v238 offset:20480
	ds_read_b128 v[52:55], v238 offset:21504
	ds_read_b128 v[56:59], v238 offset:22528
	ds_read_b128 v[60:63], v238 offset:23552
	global_load_lds_dwordx4 v[196:197], off
	v_lshl_add_u64 v[198:199], s[14:15], 0, v[208:209]
	s_mov_b32 m0, s35
	v_lshl_add_u64 v[200:201], s[14:15], 0, v[206:207]
	global_load_lds_dwordx4 v[198:199], off
	s_mov_b32 m0, s40
	v_lshl_add_u64 v[202:203], s[14:15], 0, v[210:211]
	global_load_lds_dwordx4 v[200:201], off
	s_mov_b32 m0, s41
	v_mov_b32_e32 v215, v193
	global_load_lds_dwordx4 v[202:203], off
	s_mov_b32 m0, s31
	v_lshl_add_u64 v[226:227], s[12:13], 0, v[192:193]
	global_load_lds_dwordx4 v192, s[12:13]
	s_mov_b32 m0, s53
	v_lshl_add_u64 v[228:229], s[12:13], 0, v[214:215]
	global_load_lds_dwordx4 v214, s[12:13]
	s_waitcnt vmcnt(8)
	s_waitcnt lgkmcnt(0)
	s_barrier
	s_setprio 1
	s_waitcnt lgkmcnt(0)
	v_mfma_scale_f32_16x16x128_f8f6f4 v[124:127], v[16:23], v[32:39], 0, v252, v251 op_sel_hi:[0,0,0]
	v_mfma_scale_f32_16x16x128_f8f6f4 v[116:119], v[24:31], v[32:39], 0, v252, v251 op_sel_hi:[0,0,0]
	v_mfma_scale_f32_16x16x128_f8f6f4 v[108:111], v[16:23], v[40:47], 0, v252, v251 op_sel_hi:[0,0,0]
	v_mfma_scale_f32_16x16x128_f8f6f4 v[100:103], v[24:31], v[40:47], 0, v252, v251 op_sel_hi:[0,0,0]
	v_mfma_scale_f32_16x16x128_f8f6f4 v[92:95], v[16:23], v[48:55], 0, v252, v251 op_sel_hi:[0,0,0]
	v_mfma_scale_f32_16x16x128_f8f6f4 v[84:87], v[24:31], v[48:55], 0, v252, v251 op_sel_hi:[0,0,0]
	v_mfma_scale_f32_16x16x128_f8f6f4 v[76:79], v[16:23], v[56:63], 0, v252, v251 op_sel_hi:[0,0,0]
	v_mfma_scale_f32_16x16x128_f8f6f4 v[68:71], v[24:31], v[56:63], 0, v252, v251 op_sel_hi:[0,0,0]
	s_setprio 0
	s_setprio 1
	v_mfma_scale_f32_16x16x128_f8f6f4 v[120:123], v[0:7], v[32:39], 0, v252, v251 op_sel_hi:[0,0,0]
	v_mfma_scale_f32_16x16x128_f8f6f4 v[112:115], v[8:15], v[32:39], 0, v252, v251 op_sel_hi:[0,0,0]
	v_mfma_scale_f32_16x16x128_f8f6f4 v[104:107], v[0:7], v[40:47], 0, v252, v251 op_sel_hi:[0,0,0]
	v_mfma_scale_f32_16x16x128_f8f6f4 v[96:99], v[8:15], v[40:47], 0, v252, v251 op_sel_hi:[0,0,0]
	v_mfma_scale_f32_16x16x128_f8f6f4 v[88:91], v[0:7], v[48:55], 0, v252, v251 op_sel_hi:[0,0,0]
	v_mfma_scale_f32_16x16x128_f8f6f4 v[80:83], v[8:15], v[48:55], 0, v252, v251 op_sel_hi:[0,0,0]
	v_mfma_scale_f32_16x16x128_f8f6f4 v[72:75], v[0:7], v[56:63], 0, v252, v251 op_sel_hi:[0,0,0]
	v_mfma_scale_f32_16x16x128_f8f6f4 v[64:67], v[8:15], v[56:63], 0, v252, v251 op_sel_hi:[0,0,0]
	s_setprio 0
	s_barrier
	s_add_i32 s14, 0, 0x18000
	s_add_i32 s15, 0, 0x1c000
	v_add_u32_e32 v12, s14, v236
	v_add_u32_e32 v28, s15, v236
	ds_read_b128 v[0:3], v12
	ds_read_b128 v[4:7], v12 offset:1024
	ds_read_b128 v[8:11], v12 offset:2048
	ds_read_b128 v[12:15], v12 offset:3072
	ds_read_b128 v[16:19], v28
	ds_read_b128 v[20:23], v28 offset:1024
	ds_read_b128 v[24:27], v28 offset:2048
	ds_read_b128 v[28:31], v28 offset:3072
	s_mov_b32 m0, s56
	v_lshl_add_u64 v[230:231], s[12:13], 0, v[212:213]
	ds_read_b128 v[32:35], v238 offset:32768
	ds_read_b128 v[36:39], v238 offset:33792
	ds_read_b128 v[40:43], v238 offset:34816
	ds_read_b128 v[44:47], v238 offset:35840
	ds_read_b128 v[48:51], v238 offset:36864
	ds_read_b128 v[52:55], v238 offset:37888
	ds_read_b128 v[56:59], v238 offset:38912
	ds_read_b128 v[60:63], v238 offset:39936
	global_load_lds_dwordx4 v[230:231], off
	v_lshl_add_u64 v[230:231], s[12:13], 0, v[216:217]
	s_mov_b32 m0, s57
	s_nop 0
	global_load_lds_dwordx4 v[230:231], off
	s_waitcnt vmcnt(8)
	s_waitcnt lgkmcnt(0)
	s_barrier
; #define PG8_STAGE(bufoff, gbase, voff) do { _Pragma("unroll") for (int _i = 0; _i < 2; ++_i) \
;         __builtin_amdgcn_global_load_lds((const unsigned*)((const char*)(gbase) + (voff)[_i]), (LAS unsigned*)(lds + (bufoff) + ldsw + _i * 8192), 16, 0, 0); } while (0)
; #define PG8_LDA(dst, b, h) do { _Pragma("unroll") for (int m = 0; m < 4; ++m) _Pragma("unroll") for (int k = 0; k < 2; ++k) dst[m][k] = *(const LAS bf16x8*)(lds + PG8_SA(b, h) + aoff + m * 2048 + k * KOFF); } while (0)
; #define PG8_LDB(dst, b, h) do { _Pragma("unroll") for (int n = 0; n < 2; ++n) _Pragma("unroll") for (int k = 0; k < 2; ++k) dst[n][k] = *(const LAS bf16x8*)(lds + PG8_SB(b, h) + boff + n * 2048 + k * KOFF); } while (0)
; #define PG8_WAIT_V(n) asm volatile("s_waitcnt vmcnt(" #n ")" ::: "memory")
; #define PG8_WAIT_L(n) asm volatile("s_waitcnt lgkmcnt(" #n ")" ::: "memory")
; #define PG8_BAR __builtin_amdgcn_s_barrier()
; #define PG8_SCHED __builtin_amdgcn_sched_barrier(0)
; template <class Epi, class Sched, bool GATHER, bool FP8 = false, bool ALIGN = true>
; __device__ __forceinline__ void gemm_phase(LAS unsigned char* lds, int wave, const Gemm g, const Sched& S, const Epi& E) {
;     ...
;             PG8_WAIT_V(8); PG8_WAIT_L(0); PG8_BAR; PG8_MMA(0, 0, At, B0); PG8_MMA(0, 1, At, B1); PG8_BAR; PG8_SCHED;
;             PG8_LDA(At, 0, 1); PG8_STAGE(PG8_SB(0, 0), b2, voffB0); PG8_STAGE(PG8_SB(0, 1), b2, voffB1); PG8_STAGE(PG8_SA(0, 0), a2, ca0);
;             PG8_WAIT_V(8); PG8_WAIT_L(0); PG8_BAR; PG8_MMA(1, 0, At, B0); PG8_MMA(1, 1, At, B1); PG8_BAR; PG8_SCHED;
;             PG8_LDB(B0, 1, 0); PG8_LDB(B1, 1, 1); PG8_SCHED; PG8_LDA(At, 1, 0); PG8_STAGE(PG8_SA(0, 1), a2, ca1);
;             PG8_WAIT_V(8); PG8_WAIT_L(0); PG8_BAR; PG8_MMA(0, 0, At, B0); PG8_MMA(0, 1, At, B1); PG8_BAR; PG8_SCHED;
;             PG8_LDA(At, 1, 1); PG8_STAGE(PG8_SB(1, 0), b3, voffB0); PG8_STAGE(PG8_SB(1, 1), b3, voffB1); PG8_STAGE(PG8_SA(1, 0), a3, ca0);
;             PG8_WAIT_V(8); PG8_WAIT_L(0); PG8_BAR; PG8_MMA(1, 0, At, B0); PG8_MMA(1, 1, At, B1); PG8_BAR; PG8_SCHED;
	s_setprio 1
	s_waitcnt lgkmcnt(0)
	v_mfma_scale_f32_16x16x128_f8f6f4 v[188:191], v[0:7], v[32:39], v[188:191], v252, v251 op_sel_hi:[0,0,0]
	v_mfma_scale_f32_16x16x128_f8f6f4 v[180:183], v[8:15], v[32:39], v[180:183], v252, v251 op_sel_hi:[0,0,0]
	v_mfma_scale_f32_16x16x128_f8f6f4 v[172:175], v[0:7], v[40:47], v[172:175], v252, v251 op_sel_hi:[0,0,0]
	v_mfma_scale_f32_16x16x128_f8f6f4 v[164:167], v[8:15], v[40:47], v[164:167], v252, v251 op_sel_hi:[0,0,0]
	v_mfma_scale_f32_16x16x128_f8f6f4 v[156:159], v[0:7], v[48:55], v[156:159], v252, v251 op_sel_hi:[0,0,0]
	v_mfma_scale_f32_16x16x128_f8f6f4 v[148:151], v[8:15], v[48:55], v[148:151], v252, v251 op_sel_hi:[0,0,0]
	v_mfma_scale_f32_16x16x128_f8f6f4 v[140:143], v[0:7], v[56:63], v[140:143], v252, v251 op_sel_hi:[0,0,0]
	v_mfma_scale_f32_16x16x128_f8f6f4 v[132:135], v[8:15], v[56:63], v[132:135], v252, v251 op_sel_hi:[0,0,0]
	s_setprio 0
	s_setprio 1
	v_mfma_scale_f32_16x16x128_f8f6f4 v[184:187], v[16:23], v[32:39], v[184:187], v252, v251 op_sel_hi:[0,0,0]
	v_mfma_scale_f32_16x16x128_f8f6f4 v[176:179], v[24:31], v[32:39], v[176:179], v252, v251 op_sel_hi:[0,0,0]
	v_mfma_scale_f32_16x16x128_f8f6f4 v[168:171], v[16:23], v[40:47], v[168:171], v252, v251 op_sel_hi:[0,0,0]
	v_mfma_scale_f32_16x16x128_f8f6f4 v[160:163], v[24:31], v[40:47], v[160:163], v252, v251 op_sel_hi:[0,0,0]
	v_mfma_scale_f32_16x16x128_f8f6f4 v[152:155], v[16:23], v[48:55], v[152:155], v252, v251 op_sel_hi:[0,0,0]
	v_mfma_scale_f32_16x16x128_f8f6f4 v[144:147], v[24:31], v[48:55], v[144:147], v252, v251 op_sel_hi:[0,0,0]
	v_mfma_scale_f32_16x16x128_f8f6f4 v[136:139], v[16:23], v[56:63], v[136:139], v252, v251 op_sel_hi:[0,0,0]
	v_mfma_scale_f32_16x16x128_f8f6f4 v[128:131], v[24:31], v[56:63], v[128:131], v252, v251 op_sel_hi:[0,0,0]
	s_setprio 0
	s_barrier
	s_add_i32 s12, s14, s30
	v_lshl_add_u64 v[196:197], v[196:197], 0, s[62:63]
	s_mov_b32 m0, s12
	ds_read_b128 v[32:35], v238 offset:49152
	ds_read_b128 v[36:39], v238 offset:50176
	ds_read_b128 v[40:43], v238 offset:51200
	ds_read_b128 v[44:47], v238 offset:52224
	ds_read_b128 v[48:51], v238 offset:53248
	ds_read_b128 v[52:55], v238 offset:54272
	ds_read_b128 v[56:59], v238 offset:55296
	ds_read_b128 v[60:63], v238 offset:56320
	global_load_lds_dwordx4 v[196:197], off
	v_lshl_add_u64 v[196:197], v[198:199], 0, s[62:63]
	s_add_i32 m0, s12, 0x2000
	s_add_i32 s12, s15, s30
	global_load_lds_dwordx4 v[196:197], off
	v_lshl_add_u64 v[196:197], v[200:201], 0, s[62:63]
	s_mov_b32 m0, s12
	s_nop 0
	global_load_lds_dwordx4 v[196:197], off
	v_lshl_add_u64 v[196:197], v[202:203], 0, s[62:63]
	s_add_i32 m0, s12, 0x2000
	s_nop 0
	global_load_lds_dwordx4 v[196:197], off
	v_lshl_add_u64 v[196:197], v[226:227], 0, s[62:63]
	s_mov_b32 m0, s58
	s_nop 0
	global_load_lds_dwordx4 v[196:197], off
	v_lshl_add_u64 v[196:197], v[228:229], 0, s[62:63]
	s_mov_b32 m0, s59
	s_nop 0
	global_load_lds_dwordx4 v[196:197], off
	s_waitcnt vmcnt(8)
	s_waitcnt lgkmcnt(0)
	s_barrier
	s_setprio 1
	s_waitcnt lgkmcnt(0)
	v_mfma_scale_f32_16x16x128_f8f6f4 v[124:127], v[0:7], v[32:39], v[124:127], v252, v251 op_sel_hi:[0,0,0]
	v_mfma_scale_f32_16x16x128_f8f6f4 v[116:119], v[8:15], v[32:39], v[116:119], v252, v251 op_sel_hi:[0,0,0]
	v_mfma_scale_f32_16x16x128_f8f6f4 v[108:111], v[0:7], v[40:47], v[108:111], v252, v251 op_sel_hi:[0,0,0]
	v_mfma_scale_f32_16x16x128_f8f6f4 v[100:103], v[8:15], v[40:47], v[100:103], v252, v251 op_sel_hi:[0,0,0]
	v_mfma_scale_f32_16x16x128_f8f6f4 v[92:95], v[0:7], v[48:55], v[92:95], v252, v251 op_sel_hi:[0,0,0]
	v_mfma_scale_f32_16x16x128_f8f6f4 v[84:87], v[8:15], v[48:55], v[84:87], v252, v251 op_sel_hi:[0,0,0]
	v_mfma_scale_f32_16x16x128_f8f6f4 v[76:79], v[0:7], v[56:63], v[76:79], v252, v251 op_sel_hi:[0,0,0]
	v_mfma_scale_f32_16x16x128_f8f6f4 v[68:71], v[8:15], v[56:63], v[68:71], v252, v251 op_sel_hi:[0,0,0]
	s_setprio 0
	s_setprio 1
	v_mfma_scale_f32_16x16x128_f8f6f4 v[120:123], v[16:23], v[32:39], v[120:123], v252, v251 op_sel_hi:[0,0,0]
	v_mfma_scale_f32_16x16x128_f8f6f4 v[112:115], v[24:31], v[32:39], v[112:115], v252, v251 op_sel_hi:[0,0,0]
	v_mfma_scale_f32_16x16x128_f8f6f4 v[104:107], v[16:23], v[40:47], v[104:107], v252, v251 op_sel_hi:[0,0,0]
	v_mfma_scale_f32_16x16x128_f8f6f4 v[96:99], v[24:31], v[40:47], v[96:99], v252, v251 op_sel_hi:[0,0,0]
	v_mfma_scale_f32_16x16x128_f8f6f4 v[88:91], v[16:23], v[48:55], v[88:91], v252, v251 op_sel_hi:[0,0,0]
	v_mfma_scale_f32_16x16x128_f8f6f4 v[80:83], v[24:31], v[48:55], v[80:83], v252, v251 op_sel_hi:[0,0,0]
	v_mfma_scale_f32_16x16x128_f8f6f4 v[72:75], v[16:23], v[56:63], v[72:75], v252, v251 op_sel_hi:[0,0,0]
	v_mfma_scale_f32_16x16x128_f8f6f4 v[64:67], v[24:31], v[56:63], v[64:67], v252, v251 op_sel_hi:[0,0,0]
	s_setprio 0
	s_barrier
	s_add_i32 s83, s83, 2
	s_add_u32 s10, s10, 0x100
	s_addc_u32 s11, s11, 0
	s_add_u32 s49, s49, 0x100
	s_addc_u32 s82, s82, 0
	s_cmp_gt_u32 s83, 13
	s_cbranch_scc1 .LBB0_1083
	s_branch .LBB0_1081
.LBB0_1079:
	v_mov_b32_e32 v213, v193
	v_lshl_add_u32 v192, v240, 11, v224
	v_lshl_add_u32 v212, v241, 11, v224
	v_lshl_add_u32 v214, v242, 11, v225
	v_lshl_add_u32 v216, v243, 11, v225
